# v35: v34 (wider window, 870 dead fp8-pack movs) + router bias through LDS + loop-edge drain/skip + combine3 second-row load hoist
# baseline (speedup 1.0000x reference)
.LBB0_60:
	s_waitcnt vmcnt(15)
	v_mov_b32_e32 v138, v0
	s_waitcnt vmcnt(14)
	v_mov_b32_e32 v139, v4
	v_pk_mul_f32 v[138:139], v[138:139], s[18:19] op_sel_hi:[1,0]
	s_nop 0
	v_cvt_pk_fp8_f32 v130, v138, v139
	s_waitcnt vmcnt(13)
	v_mov_b32_e32 v138, v8
	s_waitcnt vmcnt(12)
	v_mov_b32_e32 v139, v12
	v_pk_mul_f32 v[138:139], v[138:139], s[18:19] op_sel_hi:[1,0]
	s_nop 0
	v_cvt_pk_fp8_f32 v130, v138, v139 op_sel:[0,0,1]
	v_mov_b32_e32 v138, v1
	v_mov_b32_e32 v139, v5
	v_pk_mul_f32 v[138:139], v[138:139], s[18:19] op_sel_hi:[1,0]
	s_nop 0
	v_cvt_pk_fp8_f32 v137, v138, v139
	v_mov_b32_e32 v138, v9
	v_mov_b32_e32 v139, v13
	v_pk_mul_f32 v[138:139], v[138:139], s[18:19] op_sel_hi:[1,0]
	s_nop 0
	v_cvt_pk_fp8_f32 v137, v138, v139 op_sel:[0,0,1]
	v_mov_b32_e32 v138, v2
	v_mov_b32_e32 v139, v6
	v_pk_mul_f32 v[138:139], v[138:139], s[18:19] op_sel_hi:[1,0]
	s_nop 0
	v_cvt_pk_fp8_f32 v140, v138, v139
	v_mov_b32_e32 v138, v10
	v_mov_b32_e32 v139, v14
	v_pk_mul_f32 v[138:139], v[138:139], s[18:19] op_sel_hi:[1,0]
	s_nop 0
	v_cvt_pk_fp8_f32 v140, v138, v139 op_sel:[0,0,1]
	v_mov_b32_e32 v138, v3
	v_mov_b32_e32 v139, v7
	v_pk_mul_f32 v[138:139], v[138:139], s[18:19] op_sel_hi:[1,0]
	s_nop 0
	v_cvt_pk_fp8_f32 v141, v138, v139
	v_mov_b32_e32 v138, v11
	v_mov_b32_e32 v139, v15
	v_pk_mul_f32 v[138:139], v[138:139], s[18:19] op_sel_hi:[1,0]
	s_nop 0
	v_cvt_pk_fp8_f32 v141, v138, v139 op_sel:[0,0,1]
	s_waitcnt vmcnt(11)
	v_mov_b32_e32 v138, v16
	s_waitcnt vmcnt(10)
	v_mov_b32_e32 v139, v20
	ds_write2_b32 v136, v130, v137 offset1:33
	ds_write2_b32 v136, v140, v141 offset0:66 offset1:99
	v_pk_mul_f32 v[138:139], v[138:139], s[18:19] op_sel_hi:[1,0]
	s_nop 0
	v_cvt_pk_fp8_f32 v130, v138, v139
	s_waitcnt vmcnt(9)
	v_mov_b32_e32 v138, v24
	s_waitcnt vmcnt(8)
	v_mov_b32_e32 v139, v28
	v_pk_mul_f32 v[138:139], v[138:139], s[18:19] op_sel_hi:[1,0]
	s_nop 0
	v_cvt_pk_fp8_f32 v130, v138, v139 op_sel:[0,0,1]
	v_mov_b32_e32 v138, v17
	v_mov_b32_e32 v139, v21
	v_pk_mul_f32 v[138:139], v[138:139], s[18:19] op_sel_hi:[1,0]
	v_mov_b32_e32 v140, v18
	v_cvt_pk_fp8_f32 v137, v138, v139
	v_mov_b32_e32 v138, v25
	v_mov_b32_e32 v139, v29
	v_pk_mul_f32 v[138:139], v[138:139], s[18:19] op_sel_hi:[1,0]
	v_mov_b32_e32 v141, v22
	v_cvt_pk_fp8_f32 v137, v138, v139 op_sel:[0,0,1]
	v_pk_mul_f32 v[140:141], v[140:141], s[18:19] op_sel_hi:[1,0]
	s_nop 0
	v_cvt_pk_fp8_f32 v139, v140, v141
	v_mov_b32_e32 v140, v26
	v_mov_b32_e32 v141, v30
	v_pk_mul_f32 v[140:141], v[140:141], s[18:19] op_sel_hi:[1,0]
	v_add_u32_e32 v138, 0x4000, v136
	v_cvt_pk_fp8_f32 v139, v140, v141 op_sel:[0,0,1]
	v_mov_b32_e32 v140, v19
	v_mov_b32_e32 v141, v23
	v_pk_mul_f32 v[140:141], v[140:141], s[18:19] op_sel_hi:[1,0]
	s_lshl_b32 s36, s1, 7
	v_cvt_pk_fp8_f32 v142, v140, v141
	v_mov_b32_e32 v140, v27
	v_mov_b32_e32 v141, v31
	v_pk_mul_f32 v[140:141], v[140:141], s[18:19] op_sel_hi:[1,0]
	s_ashr_i32 s37, s36, 31
	v_cvt_pk_fp8_f32 v142, v140, v141 op_sel:[0,0,1]
	s_waitcnt vmcnt(7)
	v_mov_b32_e32 v140, v32
	s_waitcnt vmcnt(6)
	v_mov_b32_e32 v141, v36
	v_pk_mul_f32 v[140:141], v[140:141], s[18:19] op_sel_hi:[1,0]
	ds_write2_b32 v138, v130, v137 offset0:128 offset1:161
	ds_write2_b32 v138, v139, v142 offset0:194 offset1:227
	v_cvt_pk_fp8_f32 v143, v140, v141
	s_waitcnt vmcnt(5)
	v_mov_b32_e32 v140, v40
	s_waitcnt vmcnt(4)
	v_mov_b32_e32 v141, v44
	v_pk_mul_f32 v[140:141], v[140:141], s[18:19] op_sel_hi:[1,0]
	s_nop 0
	v_cvt_pk_fp8_f32 v143, v140, v141 op_sel:[0,0,1]
	v_mov_b32_e32 v140, v33
	v_mov_b32_e32 v141, v37
	v_pk_mul_f32 v[140:141], v[140:141], s[18:19] op_sel_hi:[1,0]
	s_nop 0
	v_cvt_pk_fp8_f32 v144, v140, v141
	v_mov_b32_e32 v140, v41
	v_mov_b32_e32 v141, v45
	v_pk_mul_f32 v[140:141], v[140:141], s[18:19] op_sel_hi:[1,0]
	s_nop 0
	v_cvt_pk_fp8_f32 v144, v140, v141 op_sel:[0,0,1]
	v_mov_b32_e32 v140, v34
	v_mov_b32_e32 v141, v38
	v_pk_mul_f32 v[140:141], v[140:141], s[18:19] op_sel_hi:[1,0]
	v_add_u32_e32 v137, 0x8400, v136
	v_cvt_pk_fp8_f32 v130, v140, v141
	v_mov_b32_e32 v140, v42
	v_mov_b32_e32 v141, v46
	v_pk_mul_f32 v[140:141], v[140:141], s[18:19] op_sel_hi:[1,0]
	ds_write2_b32 v137, v143, v144 offset1:33
	v_cvt_pk_fp8_f32 v130, v140, v141 op_sel:[0,0,1]
	v_mov_b32_e32 v140, v35
	v_mov_b32_e32 v141, v39
	v_pk_mul_f32 v[140:141], v[140:141], s[18:19] op_sel_hi:[1,0]
	s_nop 0
	v_cvt_pk_fp8_f32 v139, v140, v141
	v_mov_b32_e32 v140, v43
	v_mov_b32_e32 v141, v47
	v_pk_mul_f32 v[140:141], v[140:141], s[18:19] op_sel_hi:[1,0]
	s_nop 0
	v_cvt_pk_fp8_f32 v139, v140, v141 op_sel:[0,0,1]
	s_waitcnt vmcnt(3)
	v_mov_b32_e32 v140, v64
	s_waitcnt vmcnt(2)
	v_mov_b32_e32 v141, v68
	v_pk_mul_f32 v[140:141], v[140:141], s[18:19] op_sel_hi:[1,0]
	ds_write2_b32 v137, v130, v139 offset0:66 offset1:99
	v_cvt_pk_fp8_f32 v142, v140, v141
	s_waitcnt vmcnt(1)
	v_mov_b32_e32 v140, v88
	s_waitcnt vmcnt(0)
	v_mov_b32_e32 v141, v92
	v_pk_mul_f32 v[140:141], v[140:141], s[18:19] op_sel_hi:[1,0]
	v_add_u32_e32 v139, 0xc400, v136
	v_cvt_pk_fp8_f32 v142, v140, v141 op_sel:[0,0,1]
	v_mov_b32_e32 v140, v65
	v_mov_b32_e32 v141, v69
	v_pk_mul_f32 v[140:141], v[140:141], s[18:19] op_sel_hi:[1,0]
	s_andn2_b64 vcc, exec, s[34:35]
	v_cvt_pk_fp8_f32 v143, v140, v141
	v_mov_b32_e32 v140, v89
	v_mov_b32_e32 v141, v93
	v_pk_mul_f32 v[140:141], v[140:141], s[18:19] op_sel_hi:[1,0]
	s_mov_b64 s[34:35], -1
	v_cvt_pk_fp8_f32 v143, v140, v141 op_sel:[0,0,1]
	v_mov_b32_e32 v140, v66
	v_mov_b32_e32 v141, v70
	v_pk_mul_f32 v[140:141], v[140:141], s[18:19] op_sel_hi:[1,0]
	s_nop 0
	v_cvt_pk_fp8_f32 v144, v140, v141
	v_mov_b32_e32 v140, v90
	v_mov_b32_e32 v141, v94
	v_pk_mul_f32 v[140:141], v[140:141], s[18:19] op_sel_hi:[1,0]
	s_nop 0
	v_cvt_pk_fp8_f32 v144, v140, v141 op_sel:[0,0,1]
	v_mov_b32_e32 v140, v67
	v_mov_b32_e32 v141, v71
	v_pk_mul_f32 v[140:141], v[140:141], s[18:19] op_sel_hi:[1,0]
	s_nop 0
	v_cvt_pk_fp8_f32 v145, v140, v141
	v_mov_b32_e32 v140, v91
	v_mov_b32_e32 v141, v95
	v_pk_mul_f32 v[140:141], v[140:141], s[18:19] op_sel_hi:[1,0]
	s_nop 0
	v_cvt_pk_fp8_f32 v145, v140, v141 op_sel:[0,0,1]
	v_lshl_add_u32 v140, s0, 6, v134
	ds_write2_b32 v139, v142, v143 offset0:128 offset1:161
	ds_write2_b32 v139, v144, v145 offset0:194 offset1:227
	s_waitcnt lgkmcnt(0)
	s_barrier
	ds_read2_b32 v[142:143], v135 offset1:1
	ds_read2_b32 v[144:145], v135 offset0:2 offset1:3
	v_ashrrev_i32_e32 v141, 31, v140
	v_lshlrev_b64 v[140:141], 11, v[140:141]
	v_lshl_add_u64 v[140:141], s[14:15], 0, v[140:141]
	v_lshl_add_u64 v[140:141], v[140:141], 0, s[36:37]
	v_lshl_add_u64 v[150:151], v[140:141], 0, v[132:133]
	v_add_u32_e32 v140, 0x4200, v135
	v_add_u32_e32 v141, 0x4208, v135
	ds_read2_b32 v[146:147], v140 offset1:1
	ds_read2_b32 v[148:149], v141 offset1:1
	s_waitcnt lgkmcnt(2)
	global_store_dwordx4 v[150:151], v[142:145], off nt
	s_lshl_b32 s36, s33, 7
	s_ashr_i32 s37, s36, 31
	v_lshl_add_u32 v142, s40, 6, v134
	v_ashrrev_i32_e32 v143, 31, v142
	v_lshlrev_b64 v[142:143], 11, v[142:143]
	v_lshl_add_u64 v[142:143], s[12:13], 0, v[142:143]
	v_lshl_add_u64 v[142:143], v[142:143], 0, s[36:37]
	v_lshl_add_u64 v[142:143], v[142:143], 0, v[132:133]
	s_waitcnt lgkmcnt(0)
	global_store_dwordx4 v[142:143], v[146:149], off nt
	v_add_u32_e32 v142, 0x8400, v135
	v_lshl_add_u32 v144, s41, 6, v134
	v_add_u32_e32 v143, 0x8408, v135
	ds_read2_b32 v[146:147], v142 offset1:1
	ds_read2_b32 v[148:149], v143 offset1:1
	v_ashrrev_i32_e32 v145, 31, v144
	v_lshlrev_b64 v[144:145], 11, v[144:145]
	s_lshl_b32 s36, s42, 7
	v_lshl_add_u64 v[144:145], s[22:23], 0, v[144:145]
	s_ashr_i32 s37, s36, 31
	v_lshl_add_u64 v[144:145], v[144:145], 0, s[36:37]
	v_lshl_add_u64 v[154:155], v[144:145], 0, v[132:133]
	v_add_u32_e32 v144, 0xc600, v135
	v_add_u32_e32 v145, 0xc608, v135
	ds_read2_b32 v[150:151], v144 offset1:1
	ds_read2_b32 v[152:153], v145 offset1:1
	s_waitcnt lgkmcnt(2)
	global_store_dwordx4 v[154:155], v[146:149], off nt
	s_lshl_b32 s36, s47, 7
	s_ashr_i32 s37, s36, 31
	v_lshl_add_u32 v146, s48, 6, v134
	v_ashrrev_i32_e32 v147, 31, v146
	v_lshlrev_b64 v[146:147], 11, v[146:147]
	v_lshl_add_u64 v[146:147], s[26:27], 0, v[146:147]
	v_lshl_add_u64 v[146:147], v[146:147], 0, s[36:37]
	v_lshl_add_u64 v[146:147], v[146:147], 0, v[132:133]
	s_waitcnt lgkmcnt(0)
	global_store_dwordx4 v[146:147], v[150:153], off nt
	s_barrier
	s_cbranch_vccnz .LBB0_41
	s_add_i32 s36, s43, s44
	s_cmpk_gt_i32 s36, 0x7ff
	s_cbranch_scc1 .LBB0_40
	s_cmpk_gt_i32 s36, 0x5ff
	s_cbranch_scc0 .LBB0_64
	s_add_i32 s0, s36, 0xfffffa00
	s_lshr_b32 s1, s0, 5
	s_and_b32 s0, s36, 31
	s_mov_b64 s[12:13], s[10:11]
	s_mov_b64 s[22:23], 0x800
	s_mov_b64 s[14:15], s[4:5]
	s_cbranch_execz .LBB0_65
	s_branch .LBB0_66

.Lpeel_exit_0:
	s_mul_hi_i32 s3, s24, 0x2aaaaaab
	s_lshr_b32 s5, s3, 31
	s_lshr_b32 s3, s3, 1
	s_add_i32 s3, s3, s5
	s_lshl_b32 s5, s24, 1
	s_and_b32 s5, s5, 6
	s_and_b32 s20, s12, -16
	s_lshl_b32 s3, s3, 3
	s_or_b32 s5, s5, s20
	s_add_i32 s24, s5, s3
	v_readlane_b32 s3, v252, 41
	v_mbcnt_lo_u32_b32 v0, -1, 0
	v_mbcnt_hi_u32_b32 v0, -1, v0
	s_ashr_i32 s25, s24, 31
	s_lshl_b64 s[20:21], s[24:25], 19
	v_and_or_b32 v51, v0, 15, s3
	s_lshl_b32 s3, s12, 8
	s_and_b32 s22, s3, 0xf00
	v_ashrrev_i32_e32 v50, 4, v0
	s_add_u32 s20, s87, s20
	v_readlane_b32 s3, v252, 59
	v_lshlrev_b32_e32 v0, 5, v50
	v_lshlrev_b32_e32 v50, 3, v50
	v_lshlrev_b32_e32 v132, 12, v51
	v_mov_b32_e32 v133, v1
	s_addc_u32 s21, s3, s21
	v_and_b32_e32 v130, -16, v50
	v_lshl_add_u64 v[50:51], s[20:21], 0, v[132:133]
	v_lshl_add_u64 v[50:51], v[50:51], 0, s[22:23]
	v_and_b32_e32 v0, 32, v0
	v_lshl_add_u64 v[50:51], v[50:51], 0, s[28:29]
	v_pk_mul_f32 v[52:53], v[126:127], s[68:69] op_sel_hi:[1,0]
	s_nop 0
	v_ashrrev_i32_e32 v131, 31, v130
	v_lshl_add_u64 v[50:51], v[50:51], 0, v[0:1]
	v_cvt_pk_fp8_f32 v126, v52, v53
	v_pk_mul_f32 v[52:53], v[122:123], s[68:69] op_sel_hi:[1,0]
	s_nop 0
	v_lshl_add_u64 v[134:135], v[50:51], 0, v[130:131]
	v_pk_mul_f32 v[50:51], v[128:129], s[68:69] op_sel_hi:[1,0]
	v_cvt_pk_fp8_f32 v127, v52, v53
	v_pk_mul_f32 v[52:53], v[118:119], s[68:69] op_sel_hi:[1,0]
	s_nop 0
	v_cvt_pk_fp8_f32 v128, v52, v53
	v_pk_mul_f32 v[52:53], v[114:115], s[68:69] op_sel_hi:[1,0]
	s_nop 0
	v_cvt_pk_fp8_f32 v129, v52, v53
	v_cvt_pk_fp8_f32 v126, v50, v51 op_sel:[0,0,1]
	v_pk_mul_f32 v[50:51], v[124:125], s[68:69] op_sel_hi:[1,0]
	v_pk_mul_f32 v[52:53], v[110:111], s[68:69] op_sel_hi:[1,0]
	v_cvt_pk_fp8_f32 v127, v50, v51 op_sel:[0,0,1]
	v_pk_mul_f32 v[50:51], v[120:121], s[68:69] op_sel_hi:[1,0]
	s_nop 0
	v_cvt_pk_fp8_f32 v128, v50, v51 op_sel:[0,0,1]
	v_pk_mul_f32 v[50:51], v[116:117], s[68:69] op_sel_hi:[1,0]
	v_cvt_pk_fp8_f32 v110, v52, v53
	v_pk_mul_f32 v[52:53], v[106:107], s[68:69] op_sel_hi:[1,0]
	s_nop 0
	v_cvt_pk_fp8_f32 v129, v50, v51 op_sel:[0,0,1]
	v_pk_mul_f32 v[50:51], v[112:113], s[68:69] op_sel_hi:[1,0]
	v_cvt_pk_fp8_f32 v111, v52, v53
	v_pk_mul_f32 v[52:53], v[102:103], s[68:69] op_sel_hi:[1,0]
	s_nop 0
	v_cvt_pk_fp8_f32 v112, v52, v53
	v_cvt_pk_fp8_f32 v110, v50, v51 op_sel:[0,0,1]
	v_pk_mul_f32 v[50:51], v[108:109], s[68:69] op_sel_hi:[1,0]
	v_pk_mul_f32 v[52:53], v[94:95], s[68:69] op_sel_hi:[1,0]
	v_cvt_pk_fp8_f32 v111, v50, v51 op_sel:[0,0,1]
	v_pk_mul_f32 v[50:51], v[104:105], s[68:69] op_sel_hi:[1,0]
	s_nop 0
	v_cvt_pk_fp8_f32 v112, v50, v51 op_sel:[0,0,1]
	v_pk_mul_f32 v[50:51], v[96:97], s[68:69] op_sel_hi:[1,0]
	v_pk_mul_f32 v[96:97], v[98:99], s[68:69] op_sel_hi:[1,0]
	v_pk_mul_f32 v[90:91], v[90:91], s[68:69] op_sel_hi:[1,0]
	v_cvt_pk_fp8_f32 v94, v96, v97
	s_nop 0
	v_cvt_pk_fp8_f32 v95, v90, v91
	v_pk_mul_f32 v[86:87], v[86:87], s[68:69] op_sel_hi:[1,0]
	s_nop 0
	s_nop 0
	v_cvt_pk_fp8_f32 v96, v86, v87
	v_pk_mul_f32 v[82:83], v[82:83], s[68:69] op_sel_hi:[1,0]
	s_nop 0
	v_cvt_pk_fp8_f32 v113, v52, v53
	v_pk_mul_f32 v[52:53], v[100:101], s[68:69] op_sel_hi:[1,0]
	v_cvt_pk_fp8_f32 v97, v82, v83
	v_cvt_pk_fp8_f32 v94, v52, v53 op_sel:[0,0,1]
	v_pk_mul_f32 v[52:53], v[92:93], s[68:69] op_sel_hi:[1,0]
	s_mov_b32 s5, 0x10000
	v_cvt_pk_fp8_f32 v95, v52, v53 op_sel:[0,0,1]
	v_pk_mul_f32 v[52:53], v[88:89], s[68:69] op_sel_hi:[1,0]
	v_pk_mul_f32 v[74:75], v[74:75], s[68:69] op_sel_hi:[1,0]
	v_cvt_pk_fp8_f32 v96, v52, v53 op_sel:[0,0,1]
	v_pk_mul_f32 v[52:53], v[84:85], s[68:69] op_sel_hi:[1,0]
	v_permlane32_swap_b32_e32 v94, v95
	v_cvt_pk_fp8_f32 v97, v52, v53 op_sel:[0,0,1]
	v_add_co_u32_e32 v52, vcc, s5, v134
	v_pk_mul_f32 v[70:71], v[70:71], s[68:69] op_sel_hi:[1,0]
	v_permlane32_swap_b32_e32 v96, v97
	v_addc_co_u32_e32 v53, vcc, 0, v135, vcc
	global_store_dwordx4 v[52:53], v[94:97], off
	v_pk_mul_f32 v[52:53], v[80:81], s[68:69] op_sel_hi:[1,0]
	v_pk_mul_f32 v[80:81], v[78:79], s[68:69] op_sel_hi:[1,0]
	s_nop 0
	v_cvt_pk_fp8_f32 v78, v80, v81
	s_nop 0
	v_cvt_pk_fp8_f32 v79, v74, v75
	s_nop 0
	v_cvt_pk_fp8_f32 v80, v70, v71
	v_pk_mul_f32 v[62:63], v[62:63], s[68:69] op_sel_hi:[1,0]
	s_nop 0
	v_cvt_pk_fp8_f32 v81, v62, v63
	v_cvt_pk_fp8_f32 v78, v52, v53 op_sel:[0,0,1]
	v_pk_mul_f32 v[52:53], v[76:77], s[68:69] op_sel_hi:[1,0]
	v_pk_mul_f32 v[18:19], v[18:19], s[68:69] op_sel_hi:[1,0]
	v_cvt_pk_fp8_f32 v79, v52, v53 op_sel:[0,0,1]
	v_pk_mul_f32 v[52:53], v[72:73], s[68:69] op_sel_hi:[1,0]
	v_pk_mul_f32 v[20:21], v[20:21], s[68:69] op_sel_hi:[1,0]
	v_cvt_pk_fp8_f32 v80, v52, v53 op_sel:[0,0,1]
	v_pk_mul_f32 v[52:53], v[64:65], s[68:69] op_sel_hi:[1,0]
	s_or_b32 s20, s24, 1
	v_cvt_pk_fp8_f32 v81, v52, v53 op_sel:[0,0,1]
	v_pk_mul_f32 v[52:53], v[66:67], s[68:69] op_sel_hi:[1,0]
	s_nop 0
	v_cvt_pk_fp8_f32 v67, v18, v19
	v_pk_mul_f32 v[18:19], v[48:49], s[68:69] op_sel_hi:[1,0]
	s_nop 0
	s_ashr_i32 s21, s20, 31
	v_cvt_pk_fp8_f32 v67, v20, v21 op_sel:[0,0,1]
	v_pk_mul_f32 v[20:21], v[46:47], s[68:69] op_sel_hi:[1,0]
	s_nop 0
	v_cvt_pk_fp8_f32 v46, v20, v21
	v_pk_mul_f32 v[20:21], v[42:43], s[68:69] op_sel_hi:[1,0]
	s_nop 0
	v_cvt_pk_fp8_f32 v47, v20, v21
	v_pk_mul_f32 v[20:21], v[34:35], s[68:69] op_sel_hi:[1,0]
	v_cvt_pk_fp8_f32 v46, v18, v19 op_sel:[0,0,1]
	v_cvt_pk_fp8_f32 v48, v20, v21
	v_pk_mul_f32 v[18:19], v[44:45], s[68:69] op_sel_hi:[1,0]
	v_pk_mul_f32 v[20:21], v[26:27], s[68:69] op_sel_hi:[1,0]
	v_cvt_pk_fp8_f32 v47, v18, v19 op_sel:[0,0,1]
	v_pk_mul_f32 v[18:19], v[36:37], s[68:69] op_sel_hi:[1,0]
	s_nop 0
	v_cvt_pk_fp8_f32 v48, v18, v19 op_sel:[0,0,1]
	v_pk_mul_f32 v[18:19], v[28:29], s[68:69] op_sel_hi:[1,0]
	v_pk_mul_f32 v[28:29], v[38:39], s[68:69] op_sel_hi:[1,0]
	s_nop 0
	v_cvt_pk_fp8_f32 v26, v28, v29
	v_pk_mul_f32 v[28:29], v[30:31], s[68:69] op_sel_hi:[1,0]
	v_pk_mul_f32 v[22:23], v[22:23], s[68:69] op_sel_hi:[1,0]
	v_cvt_pk_fp8_f32 v27, v28, v29
	s_nop 0
	s_lshl_b64 s[20:21], s[20:21], 19
	s_nop 0
	v_cvt_pk_fp8_f32 v28, v22, v23
	v_pk_mul_f32 v[22:23], v[164:165], s[68:69] op_sel_hi:[1,0]
	s_nop 0
	s_mov_b64 s[26:27], 0x10000
	s_add_u32 s20, s87, s20
	v_cvt_pk_fp8_f32 v49, v20, v21
	v_pk_mul_f32 v[20:21], v[40:41], s[68:69] op_sel_hi:[1,0]
	v_cvt_pk_fp8_f32 v29, v22, v23
	v_cvt_pk_fp8_f32 v113, v50, v51 op_sel:[0,0,1]
	v_lshl_add_u64 v[50:51], v[134:135], 0, s[26:27]
	v_permlane32_swap_b32_e32 v78, v79
	v_permlane32_swap_b32_e32 v80, v81
	s_addc_u32 s21, s3, s21
	v_cvt_pk_fp8_f32 v26, v20, v21 op_sel:[0,0,1]
	v_pk_mul_f32 v[20:21], v[32:33], s[68:69] op_sel_hi:[1,0]
	global_store_dwordx4 v[50:51], v[78:81], off offset:128
	v_lshl_add_u64 v[50:51], s[20:21], 0, v[132:133]
	v_cvt_pk_fp8_f32 v27, v20, v21 op_sel:[0,0,1]
	v_pk_mul_f32 v[20:21], v[24:25], s[68:69] op_sel_hi:[1,0]
	v_lshl_add_u64 v[50:51], v[50:51], 0, s[22:23]
	v_cvt_pk_fp8_f32 v28, v20, v21 op_sel:[0,0,1]
	v_pk_mul_f32 v[20:21], v[166:167], s[68:69] op_sel_hi:[1,0]
	v_lshl_add_u64 v[50:51], v[50:51], 0, s[28:29]
	v_cvt_pk_fp8_f32 v29, v20, v21 op_sel:[0,0,1]
	v_lshl_add_u64 v[50:51], v[50:51], 0, v[0:1]
	v_lshl_add_u64 v[62:63], v[50:51], 0, v[130:131]
	v_add_co_u32_e32 v20, vcc, s5, v62
	v_permlane32_swap_b32_e32 v26, v27
	v_permlane32_swap_b32_e32 v28, v29
	v_addc_co_u32_e32 v21, vcc, 0, v63, vcc
	global_store_dwordx4 v[20:21], v[26:29], off
	v_pk_mul_f32 v[20:21], v[14:15], s[68:69] op_sel_hi:[1,0]
	s_nop 0
	v_cvt_pk_fp8_f32 v14, v20, v21
	s_nop 0
	v_cvt_pk_fp8_f32 v64, v52, v53
	v_pk_mul_f32 v[52:53], v[58:59], s[68:69] op_sel_hi:[1,0]
	s_nop 0
	v_pk_mul_f32 v[16:17], v[16:17], s[68:69] op_sel_hi:[1,0]
	v_cvt_pk_fp8_f32 v65, v52, v53
	v_pk_mul_f32 v[52:53], v[54:55], s[68:69] op_sel_hi:[1,0]
	s_nop 0
	v_cvt_pk_fp8_f32 v14, v16, v17 op_sel:[0,0,1]
	v_pk_mul_f32 v[10:11], v[10:11], s[68:69] op_sel_hi:[1,0]
	s_nop 0
	v_pk_mul_f32 v[6:7], v[6:7], s[68:69] op_sel_hi:[1,0]
	s_nop 0
	v_pk_mul_f32 v[2:3], v[2:3], s[68:69] op_sel_hi:[1,0]
	s_nop 0
	v_cvt_pk_fp8_f32 v66, v52, v53
	v_cvt_pk_fp8_f32 v15, v10, v11
	v_cvt_pk_fp8_f32 v16, v6, v7
	v_cvt_pk_fp8_f32 v17, v2, v3
	v_pk_mul_f32 v[50:51], v[68:69], s[68:69] op_sel_hi:[1,0]
	v_pk_mul_f32 v[12:13], v[12:13], s[68:69] op_sel_hi:[1,0]
	v_cvt_pk_fp8_f32 v64, v50, v51 op_sel:[0,0,1]
	v_pk_mul_f32 v[50:51], v[60:61], s[68:69] op_sel_hi:[1,0]
	v_pk_mul_f32 v[8:9], v[8:9], s[68:69] op_sel_hi:[1,0]
	v_cvt_pk_fp8_f32 v65, v50, v51 op_sel:[0,0,1]
	v_pk_mul_f32 v[50:51], v[56:57], s[68:69] op_sel_hi:[1,0]
	v_pk_mul_f32 v[4:5], v[4:5], s[68:69] op_sel_hi:[1,0]
	v_cvt_pk_fp8_f32 v66, v50, v51 op_sel:[0,0,1]
	v_cvt_pk_fp8_f32 v49, v18, v19 op_sel:[0,0,1]
	v_cvt_pk_fp8_f32 v15, v12, v13 op_sel:[0,0,1]
	v_cvt_pk_fp8_f32 v16, v8, v9 op_sel:[0,0,1]
	v_cvt_pk_fp8_f32 v17, v4, v5 op_sel:[0,0,1]
	v_permlane32_swap_b32_e32 v126, v127
	v_permlane32_swap_b32_e32 v128, v129
	v_permlane32_swap_b32_e32 v110, v111
	v_permlane32_swap_b32_e32 v112, v113
	v_permlane32_swap_b32_e32 v64, v65
	v_permlane32_swap_b32_e32 v66, v67
	v_permlane32_swap_b32_e32 v46, v47
	v_permlane32_swap_b32_e32 v48, v49
	v_lshl_add_u64 v[18:19], v[62:63], 0, s[26:27]
	v_permlane32_swap_b32_e32 v14, v15
	v_permlane32_swap_b32_e32 v16, v17
	s_and_b64 vcc, exec, s[10:11]
	s_mov_b32 s12, s2
	s_mov_b32 s24, s4
	s_mov_b64 s[46:47], s[8:9]
	s_mov_b64 s[26:27], s[6:7]
	global_store_dwordx4 v[134:135], v[126:129], off
	global_store_dwordx4 v[134:135], v[110:113], off offset:128
	global_store_dwordx4 v[62:63], v[64:67], off
	global_store_dwordx4 v[62:63], v[46:49], off offset:128
	global_store_dwordx4 v[18:19], v[14:17], off offset:128
	s_cbranch_vccz .LBB0_241
	v_readlane_b32 s0, v252, 50
	s_waitcnt vmcnt(0)
	v_readlane_b32 s1, v252, 51
	s_andn2_b64 vcc, exec, s[0:1]
	s_cbranch_vccnz .LBB0_253
	s_barrier

.LBB0_531:
	s_waitcnt vmcnt(31)
	v_mov_b32_e32 v130, v2
	s_waitcnt vmcnt(30)
	v_mov_b32_e32 v131, v6
	v_pk_mul_f32 v[130:131], v[130:131], s[72:73] op_sel_hi:[1,0]
	s_nop 0
	v_cvt_pk_fp8_f32 v0, v130, v131
	s_waitcnt vmcnt(29)
	v_mov_b32_e32 v130, v10
	s_waitcnt vmcnt(28)
	v_mov_b32_e32 v131, v14
	v_pk_mul_f32 v[130:131], v[130:131], s[72:73] op_sel_hi:[1,0]
	s_nop 0
	v_cvt_pk_fp8_f32 v0, v130, v131 op_sel:[0,0,1]
	v_mov_b32_e32 v130, v3
	v_mov_b32_e32 v131, v7
	v_pk_mul_f32 v[130:131], v[130:131], s[72:73] op_sel_hi:[1,0]
	s_nop 0
	v_cvt_pk_fp8_f32 v132, v130, v131
	v_mov_b32_e32 v130, v11
	v_mov_b32_e32 v131, v15
	v_pk_mul_f32 v[130:131], v[130:131], s[72:73] op_sel_hi:[1,0]
	s_nop 0
	v_cvt_pk_fp8_f32 v132, v130, v131 op_sel:[0,0,1]
	v_mov_b32_e32 v130, v4
	v_mov_b32_e32 v131, v8
	v_pk_mul_f32 v[130:131], v[130:131], s[72:73] op_sel_hi:[1,0]
	s_nop 0
	v_cvt_pk_fp8_f32 v133, v130, v131
	v_mov_b32_e32 v130, v12
	v_mov_b32_e32 v131, v16
	v_pk_mul_f32 v[130:131], v[130:131], s[72:73] op_sel_hi:[1,0]
	s_nop 0
	v_cvt_pk_fp8_f32 v133, v130, v131 op_sel:[0,0,1]
	v_mov_b32_e32 v130, v5
	v_mov_b32_e32 v131, v9
	v_pk_mul_f32 v[130:131], v[130:131], s[72:73] op_sel_hi:[1,0]
	v_add_u32_e32 v145, 0x4000, v143
	v_cvt_pk_fp8_f32 v138, v130, v131
	v_mov_b32_e32 v130, v13
	v_mov_b32_e32 v131, v17
	v_pk_mul_f32 v[130:131], v[130:131], s[72:73] op_sel_hi:[1,0]
	v_add_u32_e32 v144, 0x8400, v143
	v_cvt_pk_fp8_f32 v138, v130, v131 op_sel:[0,0,1]
	s_waitcnt vmcnt(27)
	v_mov_b32_e32 v130, v18
	s_waitcnt vmcnt(26)
	v_mov_b32_e32 v131, v22
	ds_write2_b32 v143, v0, v132 offset1:33
	ds_write2_b32 v143, v133, v138 offset0:66 offset1:99
	v_pk_mul_f32 v[130:131], v[130:131], s[72:73] op_sel_hi:[1,0]
	s_nop 0
	v_cvt_pk_fp8_f32 v0, v130, v131
	s_waitcnt vmcnt(25)
	v_mov_b32_e32 v130, v26
	s_waitcnt vmcnt(24)
	v_mov_b32_e32 v131, v30
	v_pk_mul_f32 v[130:131], v[130:131], s[72:73] op_sel_hi:[1,0]
	s_nop 0
	v_cvt_pk_fp8_f32 v0, v130, v131 op_sel:[0,0,1]
	v_mov_b32_e32 v130, v19
	v_mov_b32_e32 v131, v23
	v_pk_mul_f32 v[130:131], v[130:131], s[72:73] op_sel_hi:[1,0]
	s_nop 0
	v_cvt_pk_fp8_f32 v132, v130, v131
	v_mov_b32_e32 v130, v27
	v_mov_b32_e32 v131, v31
	v_pk_mul_f32 v[130:131], v[130:131], s[72:73] op_sel_hi:[1,0]
	s_nop 0
	v_cvt_pk_fp8_f32 v132, v130, v131 op_sel:[0,0,1]
	v_mov_b32_e32 v130, v20
	v_mov_b32_e32 v131, v24
	v_pk_mul_f32 v[130:131], v[130:131], s[72:73] op_sel_hi:[1,0]
	s_nop 0
	v_cvt_pk_fp8_f32 v133, v130, v131
	v_mov_b32_e32 v130, v28
	v_mov_b32_e32 v131, v32
	v_pk_mul_f32 v[130:131], v[130:131], s[72:73] op_sel_hi:[1,0]
	s_cmp_lt_i32 s40, 2
	v_cvt_pk_fp8_f32 v133, v130, v131 op_sel:[0,0,1]
	v_mov_b32_e32 v130, v21
	v_mov_b32_e32 v131, v25
	v_pk_mul_f32 v[130:131], v[130:131], s[72:73] op_sel_hi:[1,0]
	s_nop 0
	v_cvt_pk_fp8_f32 v138, v130, v131
	v_mov_b32_e32 v130, v29
	v_mov_b32_e32 v131, v33
	v_pk_mul_f32 v[130:131], v[130:131], s[72:73] op_sel_hi:[1,0]
	s_nop 0
	v_cvt_pk_fp8_f32 v138, v130, v131 op_sel:[0,0,1]
	s_waitcnt vmcnt(23)
	v_mov_b32_e32 v130, v50
	s_waitcnt vmcnt(22)
	v_mov_b32_e32 v131, v54
	v_pk_mul_f32 v[130:131], v[130:131], s[72:73] op_sel_hi:[1,0]
	ds_write2_b32 v145, v0, v132 offset0:128 offset1:161
	ds_write2_b32 v145, v133, v138 offset0:194 offset1:227
	v_cvt_pk_fp8_f32 v139, v130, v131
	s_waitcnt vmcnt(21)
	v_mov_b32_e32 v130, v58
	s_waitcnt vmcnt(20)
	v_mov_b32_e32 v131, v62
	v_pk_mul_f32 v[130:131], v[130:131], s[72:73] op_sel_hi:[1,0]
	s_nop 0
	v_cvt_pk_fp8_f32 v139, v130, v131 op_sel:[0,0,1]
	v_mov_b32_e32 v130, v51
	v_mov_b32_e32 v131, v55
	v_pk_mul_f32 v[130:131], v[130:131], s[72:73] op_sel_hi:[1,0]
	s_nop 0
	v_cvt_pk_fp8_f32 v146, v130, v131
	v_mov_b32_e32 v130, v59
	v_mov_b32_e32 v131, v63
	v_pk_mul_f32 v[130:131], v[130:131], s[72:73] op_sel_hi:[1,0]
	s_nop 0
	v_cvt_pk_fp8_f32 v146, v130, v131 op_sel:[0,0,1]
	v_mov_b32_e32 v130, v52
	v_mov_b32_e32 v131, v56
	v_pk_mul_f32 v[130:131], v[130:131], s[72:73] op_sel_hi:[1,0]
	s_nop 0
	v_cvt_pk_fp8_f32 v0, v130, v131
	v_mov_b32_e32 v130, v60
	v_mov_b32_e32 v131, v64
	v_pk_mul_f32 v[130:131], v[130:131], s[72:73] op_sel_hi:[1,0]
	ds_write2_b32 v144, v139, v146 offset1:33
	v_cvt_pk_fp8_f32 v0, v130, v131 op_sel:[0,0,1]
	v_mov_b32_e32 v130, v53
	v_mov_b32_e32 v131, v57
	v_pk_mul_f32 v[130:131], v[130:131], s[72:73] op_sel_hi:[1,0]
	s_nop 0
	v_cvt_pk_fp8_f32 v132, v130, v131
	v_mov_b32_e32 v130, v61
	v_mov_b32_e32 v131, v65
	v_pk_mul_f32 v[130:131], v[130:131], s[72:73] op_sel_hi:[1,0]
	v_add_u32_e32 v146, 0xc400, v143
	v_cvt_pk_fp8_f32 v132, v130, v131 op_sel:[0,0,1]
	s_waitcnt vmcnt(19)
	v_mov_b32_e32 v130, v82
	s_waitcnt vmcnt(18)
	v_mov_b32_e32 v131, v86
	v_pk_mul_f32 v[130:131], v[130:131], s[72:73] op_sel_hi:[1,0]
	ds_write2_b32 v144, v0, v132 offset0:66 offset1:99
	v_cvt_pk_fp8_f32 v133, v130, v131
	s_waitcnt vmcnt(17)
	v_mov_b32_e32 v130, v106
	s_waitcnt vmcnt(16)
	v_mov_b32_e32 v131, v110
	v_pk_mul_f32 v[130:131], v[130:131], s[72:73] op_sel_hi:[1,0]
	v_lshl_add_u32 v0, s21, 6, v140
	v_cvt_pk_fp8_f32 v133, v130, v131 op_sel:[0,0,1]
	v_mov_b32_e32 v130, v83
	v_mov_b32_e32 v131, v87
	v_pk_mul_f32 v[130:131], v[130:131], s[72:73] op_sel_hi:[1,0]
	s_nop 0
	v_cvt_pk_fp8_f32 v138, v130, v131
	v_mov_b32_e32 v130, v107
	v_mov_b32_e32 v131, v111
	v_pk_mul_f32 v[130:131], v[130:131], s[72:73] op_sel_hi:[1,0]
	s_nop 0
	v_cvt_pk_fp8_f32 v138, v130, v131 op_sel:[0,0,1]
	v_mov_b32_e32 v130, v84
	v_mov_b32_e32 v131, v88
	v_pk_mul_f32 v[130:131], v[130:131], s[72:73] op_sel_hi:[1,0]
	s_nop 0
	v_cvt_pk_fp8_f32 v139, v130, v131
	v_mov_b32_e32 v130, v108
	v_mov_b32_e32 v131, v112
	v_pk_mul_f32 v[130:131], v[130:131], s[72:73] op_sel_hi:[1,0]
	s_nop 0
	v_cvt_pk_fp8_f32 v139, v130, v131 op_sel:[0,0,1]
	v_mov_b32_e32 v130, v85
	v_mov_b32_e32 v131, v89
	v_pk_mul_f32 v[130:131], v[130:131], s[72:73] op_sel_hi:[1,0]
	s_nop 0
	v_cvt_pk_fp8_f32 v147, v130, v131
	v_mov_b32_e32 v130, v109
	v_mov_b32_e32 v131, v113
	v_pk_mul_f32 v[130:131], v[130:131], s[72:73] op_sel_hi:[1,0]
	s_nop 0
	v_cvt_pk_fp8_f32 v147, v130, v131 op_sel:[0,0,1]
	ds_write2_b32 v146, v133, v138 offset0:128 offset1:161
	ds_write2_b32 v146, v139, v147 offset0:194 offset1:227
	s_waitcnt lgkmcnt(0)
	s_barrier
	ds_read2_b32 v[130:131], v142 offset1:1
	ds_read2_b32 v[132:133], v142 offset0:2 offset1:3
	s_cbranch_scc1 .LBB0_537
	s_cmp_gt_i32 s40, 2
	s_cbranch_scc0 .LBB0_538
	s_cmp_eq_u32 s40, 3
	s_mov_b64 s[62:63], -1
	s_cbranch_scc0 .LBB0_535
	v_lshlrev_b32_e32 v138, 1, v0
	v_and_b32_e32 v139, 0x7f, v0
	s_movk_i32 s13, 0xff00
	v_and_or_b32 v138, v138, s13, v139
	s_mov_b64 s[62:63], 0

.LBB0_975:
	s_waitcnt vmcnt(31)
	v_mov_b32_e32 v134, v2
	s_waitcnt vmcnt(30)
	v_mov_b32_e32 v135, v6
	v_pk_mul_f32 v[134:135], v[134:135], s[88:89] op_sel_hi:[1,0]
	s_nop 0
	v_cvt_pk_fp8_f32 v136, v134, v135
	s_waitcnt vmcnt(29)
	v_mov_b32_e32 v134, v10
	s_waitcnt vmcnt(28)
	v_mov_b32_e32 v135, v18
	v_pk_mul_f32 v[134:135], v[134:135], s[88:89] op_sel_hi:[1,0]
	s_nop 0
	v_cvt_pk_fp8_f32 v136, v134, v135 op_sel:[0,0,1]
	v_mov_b32_e32 v134, v3
	v_mov_b32_e32 v135, v7
	v_pk_mul_f32 v[134:135], v[134:135], s[88:89] op_sel_hi:[1,0]
	s_nop 0
	v_cvt_pk_fp8_f32 v137, v134, v135
	v_mov_b32_e32 v134, v11
	v_mov_b32_e32 v135, v19
	v_pk_mul_f32 v[134:135], v[134:135], s[88:89] op_sel_hi:[1,0]
	s_nop 0
	v_cvt_pk_fp8_f32 v137, v134, v135 op_sel:[0,0,1]
	v_mov_b32_e32 v134, v4
	v_mov_b32_e32 v135, v8
	v_pk_mul_f32 v[134:135], v[134:135], s[88:89] op_sel_hi:[1,0]
	s_nop 0
	v_cvt_pk_fp8_f32 v138, v134, v135
	v_mov_b32_e32 v134, v12
	v_mov_b32_e32 v135, v20
	v_pk_mul_f32 v[134:135], v[134:135], s[88:89] op_sel_hi:[1,0]
	s_nop 0
	v_cvt_pk_fp8_f32 v138, v134, v135 op_sel:[0,0,1]
	v_mov_b32_e32 v134, v5
	v_mov_b32_e32 v135, v9
	v_pk_mul_f32 v[134:135], v[134:135], s[88:89] op_sel_hi:[1,0]
	v_add_u32_e32 v152, 0x4000, v143
	v_cvt_pk_fp8_f32 v139, v134, v135
	v_mov_b32_e32 v134, v13
	v_mov_b32_e32 v135, v21
	v_pk_mul_f32 v[134:135], v[134:135], s[88:89] op_sel_hi:[1,0]
	v_add_u32_e32 v151, 0x8400, v143
	v_cvt_pk_fp8_f32 v139, v134, v135 op_sel:[0,0,1]
	s_waitcnt vmcnt(27)
	v_mov_b32_e32 v134, v22
	s_waitcnt vmcnt(26)
	v_mov_b32_e32 v135, v26
	ds_write2_b32 v143, v136, v137 offset1:33
	ds_write2_b32 v143, v138, v139 offset0:66 offset1:99
	v_pk_mul_f32 v[134:135], v[134:135], s[88:89] op_sel_hi:[1,0]
	s_nop 0
	v_cvt_pk_fp8_f32 v136, v134, v135
	s_waitcnt vmcnt(25)
	v_mov_b32_e32 v134, v30
	s_waitcnt vmcnt(24)
	v_mov_b32_e32 v135, v34
	v_pk_mul_f32 v[134:135], v[134:135], s[88:89] op_sel_hi:[1,0]
	s_nop 0
	v_cvt_pk_fp8_f32 v136, v134, v135 op_sel:[0,0,1]
	v_mov_b32_e32 v134, v23
	v_mov_b32_e32 v135, v27
	v_pk_mul_f32 v[134:135], v[134:135], s[88:89] op_sel_hi:[1,0]
	s_nop 0
	v_cvt_pk_fp8_f32 v137, v134, v135
	v_mov_b32_e32 v134, v31
	v_mov_b32_e32 v135, v35
	v_pk_mul_f32 v[134:135], v[134:135], s[88:89] op_sel_hi:[1,0]
	s_nop 0
	v_cvt_pk_fp8_f32 v137, v134, v135 op_sel:[0,0,1]
	v_mov_b32_e32 v134, v24
	v_mov_b32_e32 v135, v28
	v_pk_mul_f32 v[134:135], v[134:135], s[88:89] op_sel_hi:[1,0]
	s_nop 0
	v_cvt_pk_fp8_f32 v138, v134, v135
	v_mov_b32_e32 v134, v32
	v_mov_b32_e32 v135, v36
	v_pk_mul_f32 v[134:135], v[134:135], s[88:89] op_sel_hi:[1,0]
	s_cmp_lt_i32 s41, 2
	v_cvt_pk_fp8_f32 v138, v134, v135 op_sel:[0,0,1]
	v_mov_b32_e32 v134, v25
	v_mov_b32_e32 v135, v29
	v_pk_mul_f32 v[134:135], v[134:135], s[88:89] op_sel_hi:[1,0]
	s_nop 0
	v_cvt_pk_fp8_f32 v139, v134, v135
	v_mov_b32_e32 v134, v33
	v_mov_b32_e32 v135, v37
	v_pk_mul_f32 v[134:135], v[134:135], s[88:89] op_sel_hi:[1,0]
	s_nop 0
	v_cvt_pk_fp8_f32 v139, v134, v135 op_sel:[0,0,1]
	s_waitcnt vmcnt(23)
	v_mov_b32_e32 v134, v54
	s_waitcnt vmcnt(22)
	v_mov_b32_e32 v135, v58
	v_pk_mul_f32 v[134:135], v[134:135], s[88:89] op_sel_hi:[1,0]
	ds_write2_b32 v152, v136, v137 offset0:128 offset1:161
	ds_write2_b32 v152, v138, v139 offset0:194 offset1:227
	v_cvt_pk_fp8_f32 v144, v134, v135
	s_waitcnt vmcnt(21)
	v_mov_b32_e32 v134, v62
	s_waitcnt vmcnt(20)
	v_mov_b32_e32 v135, v66
	v_pk_mul_f32 v[134:135], v[134:135], s[88:89] op_sel_hi:[1,0]
	s_nop 0
	v_cvt_pk_fp8_f32 v144, v134, v135 op_sel:[0,0,1]
	v_mov_b32_e32 v134, v55
	v_mov_b32_e32 v135, v59
	v_pk_mul_f32 v[134:135], v[134:135], s[88:89] op_sel_hi:[1,0]
	s_nop 0
	v_cvt_pk_fp8_f32 v145, v134, v135
	v_mov_b32_e32 v134, v63
	v_mov_b32_e32 v135, v67
	v_pk_mul_f32 v[134:135], v[134:135], s[88:89] op_sel_hi:[1,0]
	s_nop 0
	v_cvt_pk_fp8_f32 v145, v134, v135 op_sel:[0,0,1]
	v_mov_b32_e32 v134, v56
	v_mov_b32_e32 v135, v60
	v_pk_mul_f32 v[134:135], v[134:135], s[88:89] op_sel_hi:[1,0]
	s_nop 0
	v_cvt_pk_fp8_f32 v136, v134, v135
	v_mov_b32_e32 v134, v64
	v_mov_b32_e32 v135, v68
	v_pk_mul_f32 v[134:135], v[134:135], s[88:89] op_sel_hi:[1,0]
	ds_write2_b32 v151, v144, v145 offset1:33
	v_cvt_pk_fp8_f32 v136, v134, v135 op_sel:[0,0,1]
	v_mov_b32_e32 v134, v57
	v_mov_b32_e32 v135, v61
	v_pk_mul_f32 v[134:135], v[134:135], s[88:89] op_sel_hi:[1,0]
	s_nop 0
	v_cvt_pk_fp8_f32 v137, v134, v135
	v_mov_b32_e32 v134, v65
	v_mov_b32_e32 v135, v69
	v_pk_mul_f32 v[134:135], v[134:135], s[88:89] op_sel_hi:[1,0]
	v_add_u32_e32 v144, 0xc400, v143
	v_cvt_pk_fp8_f32 v137, v134, v135 op_sel:[0,0,1]
	s_waitcnt vmcnt(19)
	v_mov_b32_e32 v134, v102
	s_waitcnt vmcnt(18)
	v_mov_b32_e32 v135, v106
	v_pk_mul_f32 v[134:135], v[134:135], s[88:89] op_sel_hi:[1,0]
	ds_write2_b32 v151, v136, v137 offset0:66 offset1:99
	v_cvt_pk_fp8_f32 v138, v134, v135
	s_waitcnt vmcnt(17)
	v_mov_b32_e32 v134, v110
	s_waitcnt vmcnt(16)
	v_mov_b32_e32 v135, v114
	v_pk_mul_f32 v[134:135], v[134:135], s[88:89] op_sel_hi:[1,0]
	s_nop 0
	v_cvt_pk_fp8_f32 v138, v134, v135 op_sel:[0,0,1]
	v_mov_b32_e32 v134, v103
	v_mov_b32_e32 v135, v107
	v_pk_mul_f32 v[134:135], v[134:135], s[88:89] op_sel_hi:[1,0]
	s_nop 0
	v_cvt_pk_fp8_f32 v139, v134, v135
	v_mov_b32_e32 v134, v111
	v_mov_b32_e32 v135, v115
	v_pk_mul_f32 v[134:135], v[134:135], s[88:89] op_sel_hi:[1,0]
	s_nop 0
	v_cvt_pk_fp8_f32 v139, v134, v135 op_sel:[0,0,1]
	v_mov_b32_e32 v134, v104
	v_mov_b32_e32 v135, v108
	v_pk_mul_f32 v[134:135], v[134:135], s[88:89] op_sel_hi:[1,0]
	s_nop 0
	v_cvt_pk_fp8_f32 v145, v134, v135
	v_mov_b32_e32 v134, v112
	v_mov_b32_e32 v135, v116
	v_pk_mul_f32 v[134:135], v[134:135], s[88:89] op_sel_hi:[1,0]
	s_nop 0
	v_cvt_pk_fp8_f32 v145, v134, v135 op_sel:[0,0,1]
	v_mov_b32_e32 v134, v105
	v_mov_b32_e32 v135, v109
	v_pk_mul_f32 v[134:135], v[134:135], s[88:89] op_sel_hi:[1,0]
	s_nop 0
	v_cvt_pk_fp8_f32 v146, v134, v135
	v_mov_b32_e32 v134, v113
	v_mov_b32_e32 v135, v117
	v_pk_mul_f32 v[134:135], v[134:135], s[88:89] op_sel_hi:[1,0]
	s_nop 0
	v_cvt_pk_fp8_f32 v146, v134, v135 op_sel:[0,0,1]
	ds_write2_b32 v144, v138, v139 offset0:128 offset1:161
	ds_write2_b32 v144, v145, v146 offset0:194 offset1:227
	s_waitcnt lgkmcnt(0)
	s_barrier
	ds_read2_b32 v[134:135], v142 offset1:1
	ds_read2_b32 v[136:137], v142 offset0:2 offset1:3
	v_lshl_add_u32 v139, s1, 6, v140
	s_cbranch_scc1 .LBB0_981
	s_cmp_gt_i32 s41, 2
	s_cbranch_scc0 .LBB0_982
	s_cmp_eq_u32 s41, 3
	s_mov_b64 s[52:53], -1
	s_cbranch_scc0 .LBB0_979
	v_lshlrev_b32_e32 v138, 1, v139
	v_and_b32_e32 v145, 0x7f, v139
	s_movk_i32 s15, 0xff00
	v_and_or_b32 v138, v138, s15, v145
	s_mov_b64 s[52:53], 0

.LBB0_1294:
	s_waitcnt vmcnt(0)
	v_mov_b32_e32 v128, v0
	s_waitcnt vmcnt(14)
	v_mov_b32_e32 v129, v4
	v_pk_mul_f32 v[128:129], v[128:129], s[50:51] op_sel_hi:[1,0]
	s_nop 0
	v_cvt_pk_fp8_f32 v130, v128, v129
	s_waitcnt vmcnt(13)
	v_mov_b32_e32 v128, v8
	s_waitcnt vmcnt(12)
	v_mov_b32_e32 v129, v12
	v_pk_mul_f32 v[128:129], v[128:129], s[50:51] op_sel_hi:[1,0]
	s_nop 0
	v_cvt_pk_fp8_f32 v130, v128, v129 op_sel:[0,0,1]
	v_mov_b32_e32 v128, v1
	v_mov_b32_e32 v129, v5
	v_pk_mul_f32 v[128:129], v[128:129], s[50:51] op_sel_hi:[1,0]
	s_nop 0
	v_cvt_pk_fp8_f32 v131, v128, v129
	v_mov_b32_e32 v128, v9
	v_mov_b32_e32 v129, v13
	v_pk_mul_f32 v[128:129], v[128:129], s[50:51] op_sel_hi:[1,0]
	s_nop 0
	v_cvt_pk_fp8_f32 v131, v128, v129 op_sel:[0,0,1]
	v_mov_b32_e32 v128, v2
	v_mov_b32_e32 v129, v6
	v_pk_mul_f32 v[128:129], v[128:129], s[50:51] op_sel_hi:[1,0]
	s_nop 0
	v_cvt_pk_fp8_f32 v132, v128, v129
	v_mov_b32_e32 v128, v10
	v_mov_b32_e32 v129, v14
	v_pk_mul_f32 v[128:129], v[128:129], s[50:51] op_sel_hi:[1,0]
	s_nop 0
	v_cvt_pk_fp8_f32 v132, v128, v129 op_sel:[0,0,1]
	v_mov_b32_e32 v128, v3
	v_mov_b32_e32 v129, v7
	v_pk_mul_f32 v[128:129], v[128:129], s[50:51] op_sel_hi:[1,0]
	v_add_u32_e32 v151, 0x4000, v149
	v_cvt_pk_fp8_f32 v140, v128, v129
	v_mov_b32_e32 v128, v11
	v_mov_b32_e32 v129, v15
	v_pk_mul_f32 v[128:129], v[128:129], s[50:51] op_sel_hi:[1,0]
	v_add_u32_e32 v150, 0x8400, v149
	v_cvt_pk_fp8_f32 v140, v128, v129 op_sel:[0,0,1]
	s_waitcnt vmcnt(11)
	v_mov_b32_e32 v128, v16
	s_waitcnt vmcnt(10)
	v_mov_b32_e32 v129, v20
	ds_write2_b32 v149, v130, v131 offset1:33
	ds_write2_b32 v149, v132, v140 offset0:66 offset1:99
	v_pk_mul_f32 v[128:129], v[128:129], s[50:51] op_sel_hi:[1,0]
	s_nop 0
	v_cvt_pk_fp8_f32 v130, v128, v129
	s_waitcnt vmcnt(9)
	v_mov_b32_e32 v128, v24
	s_waitcnt vmcnt(8)
	v_mov_b32_e32 v129, v28
	v_pk_mul_f32 v[128:129], v[128:129], s[50:51] op_sel_hi:[1,0]
	s_nop 0
	v_cvt_pk_fp8_f32 v130, v128, v129 op_sel:[0,0,1]
	v_mov_b32_e32 v128, v17
	v_mov_b32_e32 v129, v21
	v_pk_mul_f32 v[128:129], v[128:129], s[50:51] op_sel_hi:[1,0]
	s_nop 0
	v_cvt_pk_fp8_f32 v131, v128, v129
	v_mov_b32_e32 v128, v25
	v_mov_b32_e32 v129, v29
	v_pk_mul_f32 v[128:129], v[128:129], s[50:51] op_sel_hi:[1,0]
	s_nop 0
	v_cvt_pk_fp8_f32 v131, v128, v129 op_sel:[0,0,1]
	v_mov_b32_e32 v128, v18
	v_mov_b32_e32 v129, v22
	v_pk_mul_f32 v[128:129], v[128:129], s[50:51] op_sel_hi:[1,0]
	s_nop 0
	v_cvt_pk_fp8_f32 v132, v128, v129
	v_mov_b32_e32 v128, v26
	v_mov_b32_e32 v129, v30
	v_pk_mul_f32 v[128:129], v[128:129], s[50:51] op_sel_hi:[1,0]
	s_cmp_lt_i32 s55, 2
	v_cvt_pk_fp8_f32 v132, v128, v129 op_sel:[0,0,1]
	v_mov_b32_e32 v128, v19
	v_mov_b32_e32 v129, v23
	v_pk_mul_f32 v[128:129], v[128:129], s[50:51] op_sel_hi:[1,0]
	s_nop 0
	v_cvt_pk_fp8_f32 v140, v128, v129
	v_mov_b32_e32 v128, v27
	v_mov_b32_e32 v129, v31
	v_pk_mul_f32 v[128:129], v[128:129], s[50:51] op_sel_hi:[1,0]
	s_nop 0
	v_cvt_pk_fp8_f32 v140, v128, v129 op_sel:[0,0,1]
	s_waitcnt vmcnt(7)
	v_mov_b32_e32 v128, v48
	s_waitcnt vmcnt(6)
	v_mov_b32_e32 v129, v52
	v_pk_mul_f32 v[128:129], v[128:129], s[50:51] op_sel_hi:[1,0]
	ds_write2_b32 v151, v130, v131 offset0:128 offset1:161
	ds_write2_b32 v151, v132, v140 offset0:194 offset1:227
	v_cvt_pk_fp8_f32 v141, v128, v129
	s_waitcnt vmcnt(5)
	v_mov_b32_e32 v128, v56
	s_waitcnt vmcnt(4)
	v_mov_b32_e32 v129, v60
	v_pk_mul_f32 v[128:129], v[128:129], s[50:51] op_sel_hi:[1,0]
	s_nop 0
	v_cvt_pk_fp8_f32 v141, v128, v129 op_sel:[0,0,1]
	v_mov_b32_e32 v128, v49
	v_mov_b32_e32 v129, v53
	v_pk_mul_f32 v[128:129], v[128:129], s[50:51] op_sel_hi:[1,0]
	s_nop 0
	v_cvt_pk_fp8_f32 v152, v128, v129
	v_mov_b32_e32 v128, v57
	v_mov_b32_e32 v129, v61
	v_pk_mul_f32 v[128:129], v[128:129], s[50:51] op_sel_hi:[1,0]
	s_nop 0
	v_cvt_pk_fp8_f32 v152, v128, v129 op_sel:[0,0,1]
	v_mov_b32_e32 v128, v50
	v_mov_b32_e32 v129, v54
	v_pk_mul_f32 v[128:129], v[128:129], s[50:51] op_sel_hi:[1,0]
	s_nop 0
	v_cvt_pk_fp8_f32 v130, v128, v129
	v_mov_b32_e32 v128, v58
	v_mov_b32_e32 v129, v62
	v_pk_mul_f32 v[128:129], v[128:129], s[50:51] op_sel_hi:[1,0]
	ds_write2_b32 v150, v141, v152 offset1:33
	v_cvt_pk_fp8_f32 v130, v128, v129 op_sel:[0,0,1]
	v_mov_b32_e32 v128, v51
	v_mov_b32_e32 v129, v55
	v_pk_mul_f32 v[128:129], v[128:129], s[50:51] op_sel_hi:[1,0]
	s_nop 0
	v_cvt_pk_fp8_f32 v131, v128, v129
	v_mov_b32_e32 v128, v59
	v_mov_b32_e32 v129, v63
	v_pk_mul_f32 v[128:129], v[128:129], s[50:51] op_sel_hi:[1,0]
	v_add_u32_e32 v152, 0xc400, v149
	v_cvt_pk_fp8_f32 v131, v128, v129 op_sel:[0,0,1]
	s_waitcnt vmcnt(3)
	v_mov_b32_e32 v128, v96
	s_waitcnt vmcnt(2)
	v_mov_b32_e32 v129, v100
	v_pk_mul_f32 v[128:129], v[128:129], s[50:51] op_sel_hi:[1,0]
	ds_write2_b32 v150, v130, v131 offset0:66 offset1:99
	v_cvt_pk_fp8_f32 v132, v128, v129
	s_waitcnt vmcnt(1)
	v_mov_b32_e32 v128, v104
	s_waitcnt vmcnt(0)
	v_mov_b32_e32 v129, v108
	v_pk_mul_f32 v[128:129], v[128:129], s[50:51] op_sel_hi:[1,0]
	s_nop 0
	v_cvt_pk_fp8_f32 v132, v128, v129 op_sel:[0,0,1]
	v_mov_b32_e32 v128, v97
	v_mov_b32_e32 v129, v101
	v_pk_mul_f32 v[128:129], v[128:129], s[50:51] op_sel_hi:[1,0]
	s_nop 0
	v_cvt_pk_fp8_f32 v140, v128, v129
	v_mov_b32_e32 v128, v105
	v_mov_b32_e32 v129, v109
	v_pk_mul_f32 v[128:129], v[128:129], s[50:51] op_sel_hi:[1,0]
	s_nop 0
	v_cvt_pk_fp8_f32 v140, v128, v129 op_sel:[0,0,1]
	v_mov_b32_e32 v128, v98
	v_mov_b32_e32 v129, v102
	v_pk_mul_f32 v[128:129], v[128:129], s[50:51] op_sel_hi:[1,0]
	s_nop 0
	v_cvt_pk_fp8_f32 v141, v128, v129
	v_mov_b32_e32 v128, v106
	v_mov_b32_e32 v129, v110
	v_pk_mul_f32 v[128:129], v[128:129], s[50:51] op_sel_hi:[1,0]
	s_nop 0
	v_cvt_pk_fp8_f32 v141, v128, v129 op_sel:[0,0,1]
	v_mov_b32_e32 v128, v99
	v_mov_b32_e32 v129, v103
	v_pk_mul_f32 v[128:129], v[128:129], s[50:51] op_sel_hi:[1,0]
	s_nop 0
	v_cvt_pk_fp8_f32 v153, v128, v129
	v_mov_b32_e32 v128, v107
	v_mov_b32_e32 v129, v111
	v_pk_mul_f32 v[128:129], v[128:129], s[50:51] op_sel_hi:[1,0]
	s_nop 0
	v_cvt_pk_fp8_f32 v153, v128, v129 op_sel:[0,0,1]
	ds_write2_b32 v152, v132, v140 offset0:128 offset1:161
	ds_write2_b32 v152, v141, v153 offset0:194 offset1:227
	s_waitcnt lgkmcnt(0)
	s_barrier
	ds_read2_b32 v[128:129], v148 offset1:1
	ds_read2_b32 v[130:131], v148 offset0:2 offset1:3
	v_lshl_add_u32 v132, s1, 6, v142
	s_cbranch_scc1 .LBB0_1300
	s_cmp_gt_i32 s55, 2
	s_cbranch_scc0 .LBB0_1301
	s_cmp_eq_u32 s55, 3
	s_mov_b64 s[38:39], -1
	s_cbranch_scc0 .LBB0_1298
	v_lshlrev_b32_e32 v140, 1, v132
	v_and_b32_e32 v141, 0x7f, v132
	s_movk_i32 s5, 0xff00
	v_and_or_b32 v140, v140, s5, v141
	s_mov_b64 s[38:39], 0

.Lpf_skip_0:
	v_lshlrev_b32_e32 v90, 16, v88
	v_and_b32_e32 v91, 0xffff0000, v88
	v_sub_f32_e32 v90, v86, v90
	v_sub_f32_e32 v91, v87, v91
	v_cvt_pk_bf16_f32 v89, v84, v85
	v_cvt_pk_bf16_f32 v90, v90, v91
	v_lshlrev_b32_e32 v128, 4, v128
	v_lshlrev_b32_e32 v91, 16, v89
	v_sub_f32_e32 v91, v84, v91
	v_and_b32_e32 v129, 0xffff0000, v89
	v_add3_u32 v128, s46, v128, v228
	v_sub_f32_e32 v129, v85, v129
	v_cvt_pk_bf16_f32 v91, v91, v129
	ds_write_b64 v128, v[88:89]
	v_add_u32_e32 v88, 0x10000, v128
	ds_write_b64 v88, v[90:91]
	s_nop 0
	v_cvt_pk_fp8_f32 v90, v154, v155
	s_nop 0
	v_cvt_pk_fp8_f32 v91, v174, v175
	v_lshl_add_u64 v[88:89], s[6:7], 0, v[78:79]
	v_cvt_pk_fp8_f32 v90, v152, v153 op_sel:[0,0,1]
	s_nop 0
	v_cvt_pk_fp8_f32 v91, v170, v171 op_sel:[0,0,1]
	v_cvt_pk_fp8_f32 v128, v186, v187
	global_store_dword v[88:89], v90, off
	v_lshl_add_u64 v[88:89], s[6:7], 0, v[76:77]
	s_nop 0
	global_store_dword v[88:89], v91, off
	v_cvt_pk_fp8_f32 v90, v158, v159
	s_nop 0
	v_cvt_pk_fp8_f32 v91, v178, v179
	v_cvt_pk_fp8_f32 v128, v184, v185 op_sel:[0,0,1]
	v_cvt_pk_fp8_f32 v90, v156, v157 op_sel:[0,0,1]
	v_lshl_add_u64 v[88:89], s[6:7], 0, v[74:75]
	v_cvt_pk_fp8_f32 v91, v176, v177 op_sel:[0,0,1]
	global_store_dword v[88:89], v128, off
	v_lshl_add_u64 v[88:89], s[6:7], 0, v[72:73]
	s_nop 0
	global_store_dword v[88:89], v90, off
	v_lshl_add_u64 v[88:89], s[6:7], 0, v[70:71]
	v_cvt_pk_fp8_f32 v128, v134, v135
	global_store_dword v[88:89], v91, off
	s_nop 0
	v_cvt_pk_fp8_f32 v88, v240, v241
	s_nop 0
	v_cvt_pk_fp8_f32 v89, v80, v81
	v_cvt_pk_fp8_f32 v128, v130, v131 op_sel:[0,0,1]
	v_cvt_pk_fp8_f32 v88, v238, v239 op_sel:[0,0,1]
	v_lshl_add_u64 v[80:81], s[6:7], 0, v[68:69]
	v_cvt_pk_fp8_f32 v89, v82, v83 op_sel:[0,0,1]
	global_store_dword v[80:81], v128, off
	v_lshl_add_u64 v[80:81], s[6:7], 0, v[66:67]
	global_store_dword v[80:81], v88, off
	v_lshl_add_u64 v[80:81], s[6:7], 0, v[64:65]
	global_store_dword v[80:81], v89, off
	s_nop 0
	s_nop 0
	v_cvt_pk_fp8_f32 v80, v146, v147
	v_cvt_pk_fp8_f32 v81, v164, v165
	s_add_i32 s6, s1, s18
	s_ashr_i32 s7, s6, 31
	s_lshl_b64 s[6:7], s[6:7], 11
	v_cvt_pk_fp8_f32 v80, v136, v137 op_sel:[0,0,1]
	v_cvt_pk_fp8_f32 v81, v162, v163 op_sel:[0,0,1]
	s_add_u32 s6, s41, s6
	s_addc_u32 s7, s42, s7
	v_lshl_add_u64 v[78:79], s[6:7], 0, v[78:79]
	v_lshl_add_u64 v[76:77], s[6:7], 0, v[76:77]
	s_nop 0
	global_store_dword v[78:79], v80, off
	global_store_dword v[76:77], v81, off
	s_nop 0
	s_nop 0
	v_cvt_pk_fp8_f32 v82, v182, v183
	v_cvt_pk_fp8_f32 v76, v150, v151
	v_cvt_pk_fp8_f32 v77, v172, v173
	v_lshl_add_u64 v[74:75], s[6:7], 0, v[74:75]
	v_cvt_pk_fp8_f32 v82, v180, v181 op_sel:[0,0,1]
	v_cvt_pk_fp8_f32 v76, v148, v149 op_sel:[0,0,1]
	v_cvt_pk_fp8_f32 v77, v168, v169 op_sel:[0,0,1]
	v_lshl_add_u64 v[72:73], s[6:7], 0, v[72:73]
	v_lshl_add_u64 v[70:71], s[6:7], 0, v[70:71]
	global_store_dword v[74:75], v82, off
	s_nop 0
	global_store_dword v[72:73], v76, off
	global_store_dword v[70:71], v77, off
	s_nop 0
	s_nop 0
	v_cvt_pk_fp8_f32 v74, v94, v95
	v_cvt_pk_fp8_f32 v70, v140, v141
	v_cvt_pk_fp8_f32 v71, v86, v87
	v_lshl_add_u64 v[68:69], s[6:7], 0, v[68:69]
	v_cvt_pk_fp8_f32 v74, v92, v93 op_sel:[0,0,1]
	v_cvt_pk_fp8_f32 v70, v138, v139 op_sel:[0,0,1]
	v_cvt_pk_fp8_f32 v71, v84, v85 op_sel:[0,0,1]
	v_lshl_add_u64 v[66:67], s[6:7], 0, v[66:67]
	v_lshl_add_u64 v[64:65], s[6:7], 0, v[64:65]
	global_store_dword v[68:69], v74, off
	global_store_dword v[66:67], v70, off
	global_store_dword v[64:65], v71, off
	s_waitcnt lgkmcnt(0)
	s_barrier
	ds_read_b128 v[64:67], v190
	ds_read_b128 v[68:71], v191
	s_waitcnt lgkmcnt(1)
	v_mfma_f32_16x16x32_bf16 v[72:75], v[0:3], v[64:67], 0
	v_mov_b32_e32 v128, v167
	v_mfma_f32_16x16x32_bf16 v[64:67], v[4:7], v[64:67], v[72:75]
	s_waitcnt lgkmcnt(0)
	v_mfma_f32_16x16x32_bf16 v[64:67], v[0:3], v[68:71], v[64:67]
	ds_read_b128 v[68:71], v192
	s_nop 2
	ds_read_b128 v[72:75], v193
	s_waitcnt lgkmcnt(1)
	v_mfma_f32_16x16x32_bf16 v[64:67], v[8:11], v[68:71], v[64:67]
	v_mfma_f32_16x16x32_bf16 v[64:67], v[12:15], v[68:71], v[64:67]
	s_waitcnt lgkmcnt(0)
	v_mfma_f32_16x16x32_bf16 v[64:67], v[8:11], v[72:75], v[64:67]
	ds_read_b128 v[68:71], v194
	ds_read_b128 v[72:75], v195
	s_waitcnt lgkmcnt(1)
	v_mfma_f32_16x16x32_bf16 v[64:67], v[16:19], v[68:71], v[64:67]
	v_mfma_f32_16x16x32_bf16 v[64:67], v[20:23], v[68:71], v[64:67]
	s_waitcnt lgkmcnt(0)
	v_mfma_f32_16x16x32_bf16 v[64:67], v[16:19], v[72:75], v[64:67]
	ds_read_b128 v[68:71], v196
	ds_read_b128 v[72:75], v197
	s_waitcnt lgkmcnt(1)
	v_mfma_f32_16x16x32_bf16 v[64:67], v[24:27], v[68:71], v[64:67]
	v_mfma_f32_16x16x32_bf16 v[64:67], v[28:31], v[68:71], v[64:67]
	s_waitcnt lgkmcnt(0)
	v_mfma_f32_16x16x32_bf16 v[64:67], v[24:27], v[72:75], v[64:67]
	ds_read_b128 v[68:71], v198
	ds_read_b128 v[72:75], v199
	s_waitcnt lgkmcnt(1)
	v_mfma_f32_16x16x32_bf16 v[64:67], v[32:35], v[68:71], v[64:67]
	v_mfma_f32_16x16x32_bf16 v[64:67], v[36:39], v[68:71], v[64:67]
	s_waitcnt lgkmcnt(0)
	v_mfma_f32_16x16x32_bf16 v[64:67], v[32:35], v[72:75], v[64:67]
	ds_read_b128 v[68:71], v200
	ds_read_b128 v[72:75], v201
	s_waitcnt lgkmcnt(1)
	v_mfma_f32_16x16x32_bf16 v[64:67], v[40:43], v[68:71], v[64:67]
	v_mfma_f32_16x16x32_bf16 v[64:67], v[44:47], v[68:71], v[64:67]
	s_waitcnt lgkmcnt(0)
	v_mfma_f32_16x16x32_bf16 v[64:67], v[40:43], v[72:75], v[64:67]
	ds_read_b128 v[68:71], v202
	ds_read_b128 v[72:75], v203
	s_waitcnt lgkmcnt(1)
	v_mfma_f32_16x16x32_bf16 v[64:67], v[48:51], v[68:71], v[64:67]
	v_mfma_f32_16x16x32_bf16 v[64:67], v[52:55], v[68:71], v[64:67]
	s_waitcnt lgkmcnt(0)
	v_mfma_f32_16x16x32_bf16 v[64:67], v[48:51], v[72:75], v[64:67]
	ds_read_b128 v[68:71], v204
	ds_read_b128 v[72:75], v205
	s_waitcnt lgkmcnt(1)
	v_mfma_f32_16x16x32_bf16 v[64:67], v[56:59], v[68:71], v[64:67]
	v_mfma_f32_16x16x32_bf16 v[64:67], v[60:63], v[68:71], v[64:67]
	s_waitcnt lgkmcnt(0)
	v_mfma_f32_16x16x32_bf16 v[64:67], v[56:59], v[72:75], v[64:67]
	s_nop 7
	ds_write_b128 v208, v[64:67]
	s_waitcnt lgkmcnt(0)
	s_barrier
	s_nop 0
	v_cmp_gt_i32_e32 vcc, s48, v128
	s_and_saveexec_b64 s[6:7], vcc
	s_cbranch_execz .LBB0_1743
	v_lshl_add_u32 v72, v128, 2, 0
	v_add_u32_e32 v70, 0x22000, v72
	ds_read2st64_b32 v[64:65], v70 offset1:4
	ds_read2st64_b32 v[66:67], v70 offset0:8 offset1:12
	ds_read2st64_b32 v[68:69], v70 offset0:16 offset1:20
	ds_read2st64_b32 v[70:71], v70 offset0:24 offset1:28
	s_waitcnt lgkmcnt(3)
	v_add_f32_e32 v64, 0, v64
	v_add_f32_e32 v64, v64, v65
	s_waitcnt lgkmcnt(2)
	v_add_f32_e32 v64, v64, v66
	v_add_f32_e32 v64, v64, v67
	s_waitcnt lgkmcnt(1)
	v_add_f32_e32 v64, v64, v68
	v_add_f32_e32 v64, v64, v69
	s_waitcnt lgkmcnt(0)
	v_add_f32_e32 v64, v64, v70
	v_add_f32_e32 v64, v64, v71
	v_add_u32_e32 v65, 0x21000, v72
	ds_write_b32 v65, v64
	v_mul_f32_e32 v142, 0xbfb8aa3b, v64
	v_fma_f32 v143, v64, s50, -v142
	v_rndne_f32_e32 v144, v142
	v_fmac_f32_e32 v143, 0xb2a5705f, v64
	v_sub_f32_e32 v142, v142, v144
	v_add_f32_e32 v142, v142, v143
	v_cvt_i32_f32_e32 v145, v144
	v_exp_f32_e32 v146, v142
	v_cmp_nlt_f32_e32 vcc, s51, v64
	v_ldexp_f32 v145, v146, v145
	s_nop 0
	v_cndmask_b32_e32 v145, 0, v145, vcc
	v_cmp_ngt_f32_e32 vcc, s52, v64
	s_nop 1
	v_cndmask_b32_e32 v145, v211, v145, vcc
	v_add_f32_e32 v145, 1.0, v145
	v_div_scale_f32 v146, s[98:99], v145, v145, 1.0
	v_rcp_f32_e32 v147, v146
	v_div_scale_f32 v148, vcc, 1.0, v145, 1.0
	v_fma_f32 v149, -v146, v147, 1.0
	v_fmac_f32_e32 v147, v149, v147
	v_mul_f32_e32 v149, v148, v147
	v_fma_f32 v150, -v146, v149, v148
	v_fmac_f32_e32 v149, v150, v147
	v_fma_f32 v146, -v146, v149, v148
	v_div_fmas_f32 v146, v146, v147, v149
	v_div_fixup_f32 v146, v146, v145, 1.0
	ds_write_b32 v65, v146 offset:1024
	v_add_f32_e32 v147, v249, v146
	ds_write_b32 v65, v147 offset:2048

.LBB0_2081:
	s_waitcnt vmcnt(31)
	v_mov_b32_e32 v128, v0
	s_waitcnt vmcnt(30)
	v_mov_b32_e32 v129, v4
	v_pk_mul_f32 v[128:129], v[128:129], s[34:35] op_sel_hi:[1,0]
	s_nop 0
	v_cvt_pk_fp8_f32 v130, v128, v129
	s_waitcnt vmcnt(29)
	v_mov_b32_e32 v128, v8
	s_waitcnt vmcnt(28)
	v_mov_b32_e32 v129, v12
	v_pk_mul_f32 v[128:129], v[128:129], s[34:35] op_sel_hi:[1,0]
	s_nop 0
	v_cvt_pk_fp8_f32 v130, v128, v129 op_sel:[0,0,1]
	v_mov_b32_e32 v128, v1
	v_mov_b32_e32 v129, v5
	v_pk_mul_f32 v[128:129], v[128:129], s[34:35] op_sel_hi:[1,0]
	s_nop 0
	v_cvt_pk_fp8_f32 v131, v128, v129
	v_mov_b32_e32 v128, v9
	v_mov_b32_e32 v129, v13
	v_pk_mul_f32 v[128:129], v[128:129], s[34:35] op_sel_hi:[1,0]
	s_nop 0
	v_cvt_pk_fp8_f32 v131, v128, v129 op_sel:[0,0,1]
	v_mov_b32_e32 v128, v2
	v_mov_b32_e32 v129, v6
	v_pk_mul_f32 v[128:129], v[128:129], s[34:35] op_sel_hi:[1,0]
	s_nop 0
	v_cvt_pk_fp8_f32 v134, v128, v129
	v_mov_b32_e32 v128, v10
	v_mov_b32_e32 v129, v14
	v_pk_mul_f32 v[128:129], v[128:129], s[34:35] op_sel_hi:[1,0]
	s_nop 0
	v_cvt_pk_fp8_f32 v134, v128, v129 op_sel:[0,0,1]
	v_mov_b32_e32 v128, v3
	v_mov_b32_e32 v129, v7
	v_pk_mul_f32 v[128:129], v[128:129], s[34:35] op_sel_hi:[1,0]
	v_add_u32_e32 v145, 0x4000, v143
	v_cvt_pk_fp8_f32 v138, v128, v129
	v_mov_b32_e32 v128, v11
	v_mov_b32_e32 v129, v15
	v_pk_mul_f32 v[128:129], v[128:129], s[34:35] op_sel_hi:[1,0]
	v_add_u32_e32 v144, 0x8400, v143
	v_cvt_pk_fp8_f32 v138, v128, v129 op_sel:[0,0,1]
	s_waitcnt vmcnt(27)
	v_mov_b32_e32 v128, v16
	s_waitcnt vmcnt(26)
	v_mov_b32_e32 v129, v20
	ds_write2_b32 v143, v130, v131 offset1:33
	ds_write2_b32 v143, v134, v138 offset0:66 offset1:99
	v_pk_mul_f32 v[128:129], v[128:129], s[34:35] op_sel_hi:[1,0]
	s_nop 0
	v_cvt_pk_fp8_f32 v130, v128, v129
	s_waitcnt vmcnt(25)
	v_mov_b32_e32 v128, v24
	s_waitcnt vmcnt(24)
	v_mov_b32_e32 v129, v28
	v_pk_mul_f32 v[128:129], v[128:129], s[34:35] op_sel_hi:[1,0]
	s_nop 0
	v_cvt_pk_fp8_f32 v130, v128, v129 op_sel:[0,0,1]
	v_mov_b32_e32 v128, v17
	v_mov_b32_e32 v129, v21
	v_pk_mul_f32 v[128:129], v[128:129], s[34:35] op_sel_hi:[1,0]
	s_nop 0
	v_cvt_pk_fp8_f32 v131, v128, v129
	v_mov_b32_e32 v128, v25
	v_mov_b32_e32 v129, v29
	v_pk_mul_f32 v[128:129], v[128:129], s[34:35] op_sel_hi:[1,0]
	s_nop 0
	v_cvt_pk_fp8_f32 v131, v128, v129 op_sel:[0,0,1]
	v_mov_b32_e32 v128, v18
	v_mov_b32_e32 v129, v22
	v_pk_mul_f32 v[128:129], v[128:129], s[34:35] op_sel_hi:[1,0]
	s_nop 0
	v_cvt_pk_fp8_f32 v134, v128, v129
	v_mov_b32_e32 v128, v26
	v_mov_b32_e32 v129, v30
	v_pk_mul_f32 v[128:129], v[128:129], s[34:35] op_sel_hi:[1,0]
	s_cmp_lt_i32 s78, 2
	v_cvt_pk_fp8_f32 v134, v128, v129 op_sel:[0,0,1]
	v_mov_b32_e32 v128, v19
	v_mov_b32_e32 v129, v23
	v_pk_mul_f32 v[128:129], v[128:129], s[34:35] op_sel_hi:[1,0]
	s_nop 0
	v_cvt_pk_fp8_f32 v138, v128, v129
	v_mov_b32_e32 v128, v27
	v_mov_b32_e32 v129, v31
	v_pk_mul_f32 v[128:129], v[128:129], s[34:35] op_sel_hi:[1,0]
	s_nop 0
	v_cvt_pk_fp8_f32 v138, v128, v129 op_sel:[0,0,1]
	s_waitcnt vmcnt(23)
	v_mov_b32_e32 v128, v48
	s_waitcnt vmcnt(22)
	v_mov_b32_e32 v129, v52
	v_pk_mul_f32 v[128:129], v[128:129], s[34:35] op_sel_hi:[1,0]
	ds_write2_b32 v145, v130, v131 offset0:128 offset1:161
	ds_write2_b32 v145, v134, v138 offset0:194 offset1:227
	v_cvt_pk_fp8_f32 v139, v128, v129
	s_waitcnt vmcnt(21)
	v_mov_b32_e32 v128, v56
	s_waitcnt vmcnt(20)
	v_mov_b32_e32 v129, v60
	v_pk_mul_f32 v[128:129], v[128:129], s[34:35] op_sel_hi:[1,0]
	s_nop 0
	v_cvt_pk_fp8_f32 v139, v128, v129 op_sel:[0,0,1]
	v_mov_b32_e32 v128, v49
	v_mov_b32_e32 v129, v53
	v_pk_mul_f32 v[128:129], v[128:129], s[34:35] op_sel_hi:[1,0]
	s_nop 0
	v_cvt_pk_fp8_f32 v146, v128, v129
	v_mov_b32_e32 v128, v57
	v_mov_b32_e32 v129, v61
	v_pk_mul_f32 v[128:129], v[128:129], s[34:35] op_sel_hi:[1,0]
	s_nop 0
	v_cvt_pk_fp8_f32 v146, v128, v129 op_sel:[0,0,1]
	v_mov_b32_e32 v128, v50
	v_mov_b32_e32 v129, v54
	v_pk_mul_f32 v[128:129], v[128:129], s[34:35] op_sel_hi:[1,0]
	s_nop 0
	v_cvt_pk_fp8_f32 v130, v128, v129
	v_mov_b32_e32 v128, v58
	v_mov_b32_e32 v129, v62
	v_pk_mul_f32 v[128:129], v[128:129], s[34:35] op_sel_hi:[1,0]
	ds_write2_b32 v144, v139, v146 offset1:33
	v_cvt_pk_fp8_f32 v130, v128, v129 op_sel:[0,0,1]
	v_mov_b32_e32 v128, v51
	v_mov_b32_e32 v129, v55
	v_pk_mul_f32 v[128:129], v[128:129], s[34:35] op_sel_hi:[1,0]
	s_nop 0
	v_cvt_pk_fp8_f32 v131, v128, v129
	v_mov_b32_e32 v128, v59
	v_mov_b32_e32 v129, v63
	v_pk_mul_f32 v[128:129], v[128:129], s[34:35] op_sel_hi:[1,0]
	v_add_u32_e32 v146, 0xc400, v143
	v_cvt_pk_fp8_f32 v131, v128, v129 op_sel:[0,0,1]
	s_waitcnt vmcnt(19)
	v_mov_b32_e32 v128, v96
	s_waitcnt vmcnt(18)
	v_mov_b32_e32 v129, v100
	v_pk_mul_f32 v[128:129], v[128:129], s[34:35] op_sel_hi:[1,0]
	ds_write2_b32 v144, v130, v131 offset0:66 offset1:99
	v_cvt_pk_fp8_f32 v134, v128, v129
	s_waitcnt vmcnt(17)
	v_mov_b32_e32 v128, v104
	s_waitcnt vmcnt(16)
	v_mov_b32_e32 v129, v108
	v_pk_mul_f32 v[128:129], v[128:129], s[34:35] op_sel_hi:[1,0]
	s_nop 0
	v_cvt_pk_fp8_f32 v134, v128, v129 op_sel:[0,0,1]
	v_mov_b32_e32 v128, v97
	v_mov_b32_e32 v129, v101
	v_pk_mul_f32 v[128:129], v[128:129], s[34:35] op_sel_hi:[1,0]
	s_nop 0
	v_cvt_pk_fp8_f32 v138, v128, v129
	v_mov_b32_e32 v128, v105
	v_mov_b32_e32 v129, v109
	v_pk_mul_f32 v[128:129], v[128:129], s[34:35] op_sel_hi:[1,0]
	s_nop 0
	v_cvt_pk_fp8_f32 v138, v128, v129 op_sel:[0,0,1]
	v_mov_b32_e32 v128, v98
	v_mov_b32_e32 v129, v102
	v_pk_mul_f32 v[128:129], v[128:129], s[34:35] op_sel_hi:[1,0]
	s_nop 0
	v_cvt_pk_fp8_f32 v139, v128, v129
	v_mov_b32_e32 v128, v106
	v_mov_b32_e32 v129, v110
	v_pk_mul_f32 v[128:129], v[128:129], s[34:35] op_sel_hi:[1,0]
	s_nop 0
	v_cvt_pk_fp8_f32 v139, v128, v129 op_sel:[0,0,1]
	v_mov_b32_e32 v128, v99
	v_mov_b32_e32 v129, v103
	v_pk_mul_f32 v[128:129], v[128:129], s[34:35] op_sel_hi:[1,0]
	s_nop 0
	v_cvt_pk_fp8_f32 v147, v128, v129
	v_mov_b32_e32 v128, v107
	v_mov_b32_e32 v129, v111
	v_pk_mul_f32 v[128:129], v[128:129], s[34:35] op_sel_hi:[1,0]
	s_nop 0
	v_cvt_pk_fp8_f32 v147, v128, v129 op_sel:[0,0,1]
	ds_write2_b32 v146, v134, v138 offset0:128 offset1:161
	ds_write2_b32 v146, v139, v147 offset0:194 offset1:227
	s_waitcnt lgkmcnt(0)
	s_barrier
	ds_read2_b32 v[128:129], v142 offset1:1
	ds_read2_b32 v[130:131], v142 offset0:2 offset1:3
	v_lshl_add_u32 v134, s77, 6, v140
	s_cbranch_scc1 .LBB0_2087
	s_cmp_gt_i32 s78, 2
	s_cbranch_scc0 .LBB0_2088
	s_cmp_eq_u32 s78, 3
	s_mov_b64 s[68:69], -1
	s_cbranch_scc0 .LBB0_2085
	v_lshlrev_b32_e32 v138, 1, v134
	v_and_b32_e32 v139, 0x7f, v134
	s_movk_i32 s11, 0xff00
	v_and_or_b32 v138, v138, s11, v139
	s_mov_b64 s[68:69], 0

.Lpeel_exit_4:
	v_pk_mul_f32 v[140:141], v[124:125], s[8:9] op_sel_hi:[1,0]
	v_pk_mul_f32 v[120:121], v[120:121], s[8:9] op_sel_hi:[1,0]
	s_nop 0
	v_cvt_pk_fp8_f32 v125, v120, v121
	v_pk_mul_f32 v[120:121], v[126:127], s[8:9] op_sel_hi:[1,0]
	v_pk_mul_f32 v[116:117], v[116:117], s[8:9] op_sel_hi:[1,0]
	s_nop 0
	v_cvt_pk_fp8_f32 v126, v116, v117
	v_pk_mul_f32 v[112:113], v[112:113], s[8:9] op_sel_hi:[1,0]
	s_nop 0
	v_cvt_pk_fp8_f32 v127, v112, v113
	v_pk_mul_f32 v[112:113], v[118:119], s[8:9] op_sel_hi:[1,0]
	v_pk_mul_f32 v[104:105], v[104:105], s[8:9] op_sel_hi:[1,0]
	v_cvt_pk_fp8_f32 v126, v112, v113 op_sel:[0,0,1]
	v_pk_mul_f32 v[112:113], v[114:115], s[8:9] op_sel_hi:[1,0]
	v_pk_mul_f32 v[100:101], v[100:101], s[8:9] op_sel_hi:[1,0]
	v_cvt_pk_fp8_f32 v127, v112, v113 op_sel:[0,0,1]
	v_pk_mul_f32 v[112:113], v[108:109], s[8:9] op_sel_hi:[1,0]
	s_nop 0
	v_cvt_pk_fp8_f32 v109, v104, v105
	v_pk_mul_f32 v[104:105], v[110:111], s[8:9] op_sel_hi:[1,0]
	s_nop 0
	v_cvt_pk_fp8_f32 v110, v100, v101
	v_pk_mul_f32 v[100:101], v[92:93], s[8:9] op_sel_hi:[1,0]
	v_pk_mul_f32 v[88:89], v[88:89], s[8:9] op_sel_hi:[1,0]
	s_nop 0
	v_cvt_pk_fp8_f32 v93, v88, v89
	v_pk_mul_f32 v[88:89], v[94:95], s[8:9] op_sel_hi:[1,0]
	v_pk_mul_f32 v[84:85], v[84:85], s[8:9] op_sel_hi:[1,0]
	s_nop 0
	v_cvt_pk_fp8_f32 v94, v84, v85
	v_pk_mul_f32 v[80:81], v[80:81], s[8:9] op_sel_hi:[1,0]
	s_nop 0
	v_cvt_pk_fp8_f32 v95, v80, v81
	v_pk_mul_f32 v[80:81], v[86:87], s[8:9] op_sel_hi:[1,0]
	v_pk_mul_f32 v[72:73], v[72:73], s[8:9] op_sel_hi:[1,0]
	v_cvt_pk_fp8_f32 v94, v80, v81 op_sel:[0,0,1]
	v_pk_mul_f32 v[80:81], v[82:83], s[8:9] op_sel_hi:[1,0]
	v_pk_mul_f32 v[68:69], v[68:69], s[8:9] op_sel_hi:[1,0]
	v_cvt_pk_fp8_f32 v95, v80, v81 op_sel:[0,0,1]
	v_pk_mul_f32 v[80:81], v[76:77], s[8:9] op_sel_hi:[1,0]
	s_nop 0
	v_cvt_pk_fp8_f32 v77, v72, v73
	v_pk_mul_f32 v[72:73], v[78:79], s[8:9] op_sel_hi:[1,0]
	s_nop 0
	v_cvt_pk_fp8_f32 v78, v68, v69
	v_pk_mul_f32 v[64:65], v[64:65], s[8:9] op_sel_hi:[1,0]
	s_nop 0
	v_cvt_pk_fp8_f32 v79, v64, v65
	v_pk_mul_f32 v[64:65], v[70:71], s[8:9] op_sel_hi:[1,0]
	v_pk_mul_f32 v[56:57], v[56:57], s[8:9] op_sel_hi:[1,0]
	v_cvt_pk_fp8_f32 v78, v64, v65 op_sel:[0,0,1]
	v_pk_mul_f32 v[64:65], v[66:67], s[8:9] op_sel_hi:[1,0]
	v_pk_mul_f32 v[52:53], v[52:53], s[8:9] op_sel_hi:[1,0]
	v_cvt_pk_fp8_f32 v79, v64, v65 op_sel:[0,0,1]
	v_pk_mul_f32 v[64:65], v[60:61], s[8:9] op_sel_hi:[1,0]
	s_nop 0
	v_cvt_pk_fp8_f32 v61, v56, v57
	v_pk_mul_f32 v[56:57], v[62:63], s[8:9] op_sel_hi:[1,0]
	s_nop 0
	v_cvt_pk_fp8_f32 v62, v52, v53
	v_pk_mul_f32 v[48:49], v[48:49], s[8:9] op_sel_hi:[1,0]
	s_nop 0
	v_cvt_pk_fp8_f32 v63, v48, v49
	s_lshl_b32 s16, s50, 8
	v_pk_mul_f32 v[48:49], v[54:55], s[8:9] op_sel_hi:[1,0]
	s_add_i32 s16, s16, s34
	v_cvt_pk_fp8_f32 v62, v48, v49 op_sel:[0,0,1]
	v_pk_mul_f32 v[48:49], v[50:51], s[8:9] op_sel_hi:[1,0]
	s_lshl_b32 s18, s51, 8
	s_ashr_i32 s17, s16, 31
	v_cvt_pk_fp8_f32 v63, v48, v49 op_sel:[0,0,1]
	v_pk_mul_f32 v[48:49], v[44:45], s[8:9] op_sel_hi:[1,0]
	v_pk_mul_f32 v[40:41], v[40:41], s[8:9] op_sel_hi:[1,0]
	s_nop 0
	s_ashr_i32 s19, s18, 31
	s_lshl_b64 s[20:21], s[16:17], 11
	v_cvt_pk_fp8_f32 v45, v40, v41
	v_pk_mul_f32 v[40:41], v[46:47], s[8:9] op_sel_hi:[1,0]
	v_pk_mul_f32 v[36:37], v[36:37], s[8:9] op_sel_hi:[1,0]
	s_nop 0
	s_add_u32 s17, s31, s20
	v_cvt_pk_fp8_f32 v46, v36, v37
	v_pk_mul_f32 v[36:37], v[28:29], s[8:9] op_sel_hi:[1,0]
	v_pk_mul_f32 v[24:25], v[24:25], s[8:9] op_sel_hi:[1,0]
	s_nop 0
	s_addc_u32 s20, s33, s21
	v_cvt_pk_fp8_f32 v29, v24, v25
	v_pk_mul_f32 v[24:25], v[30:31], s[8:9] op_sel_hi:[1,0]
	v_pk_mul_f32 v[20:21], v[20:21], s[8:9] op_sel_hi:[1,0]
	s_nop 0
	s_add_u32 s17, s17, s18
	v_cvt_pk_fp8_f32 v30, v20, v21
	v_pk_mul_f32 v[16:17], v[16:17], s[8:9] op_sel_hi:[1,0]
	s_nop 0
	s_addc_u32 s21, s20, s19
	v_cvt_pk_fp8_f32 v31, v16, v17
	s_add_u32 s20, s17, s35
	s_addc_u32 s21, s21, 0
	s_addk_i32 s16, 0x80
	v_pk_mul_f32 v[16:17], v[22:23], s[8:9] op_sel_hi:[1,0]
	s_ashr_i32 s17, s16, 31
	v_cvt_pk_fp8_f32 v30, v16, v17 op_sel:[0,0,1]
	v_pk_mul_f32 v[16:17], v[18:19], s[8:9] op_sel_hi:[1,0]
	s_nop 0
	s_nop 0
	v_pk_mul_f32 v[96:97], v[96:97], s[8:9] op_sel_hi:[1,0]
	s_nop 0
	s_nop 0
	s_lshl_b64 s[16:17], s[16:17], 11
	s_nop 0
	s_nop 0
	s_nop 0
	v_cvt_pk_fp8_f32 v31, v16, v17 op_sel:[0,0,1]
	v_pk_mul_f32 v[16:17], v[12:13], s[8:9] op_sel_hi:[1,0]
	v_pk_mul_f32 v[8:9], v[8:9], s[8:9] op_sel_hi:[1,0]
	s_nop 0
	v_mbcnt_lo_u32_b32 v128, -1, 0
	v_mbcnt_hi_u32_b32 v128, -1, v128
	v_cvt_pk_fp8_f32 v124, v140, v141
	v_ashrrev_i32_e32 v130, 1, v128
	v_cvt_pk_fp8_f32 v108, v112, v113
	v_cvt_pk_fp8_f32 v111, v96, v97
	v_cvt_pk_fp8_f32 v92, v100, v101
	s_nop 0
	v_cvt_pk_fp8_f32 v60, v64, v65
	v_cvt_pk_fp8_f32 v44, v48, v49
	v_pk_mul_f32 v[32:33], v[32:33], s[8:9] op_sel_hi:[1,0]
	s_nop 0
	s_add_u32 s16, s31, s16
	v_cvt_pk_fp8_f32 v28, v36, v37
	s_nop 0
	v_cvt_pk_fp8_f32 v13, v8, v9
	v_pk_mul_f32 v[8:9], v[14:15], s[8:9] op_sel_hi:[1,0]
	v_pk_mul_f32 v[4:5], v[4:5], s[8:9] op_sel_hi:[1,0]
	s_nop 0
	v_bfi_b32 v130, -16, v130, v128
	v_cvt_pk_fp8_f32 v76, v80, v81
	v_cvt_pk_fp8_f32 v47, v32, v33
	s_addc_u32 s17, s33, s17
	v_cvt_pk_fp8_f32 v12, v16, v17
	v_cvt_pk_fp8_f32 v14, v4, v5
	v_pk_mul_f32 v[0:1], v[0:1], s[8:9] op_sel_hi:[1,0]
	s_nop 0
	v_ashrrev_i32_e32 v131, 31, v130
	v_pk_mul_f32 v[96:97], v[102:103], s[8:9] op_sel_hi:[1,0]
	s_add_u32 s16, s16, s18
	v_cvt_pk_fp8_f32 v15, v0, v1
	v_lshlrev_b64 v[130:131], 11, v[130:131]
	v_cvt_pk_fp8_f32 v110, v96, v97 op_sel:[0,0,1]
	v_pk_mul_f32 v[96:97], v[98:99], s[8:9] op_sel_hi:[1,0]
	v_pk_mul_f32 v[32:33], v[38:39], s[8:9] op_sel_hi:[1,0]
	s_addc_u32 s17, s17, s19
	v_and_b32_e32 v128, 16, v128
	v_cvt_pk_fp8_f32 v124, v120, v121 op_sel:[0,0,1]
	v_pk_mul_f32 v[120:121], v[122:123], s[8:9] op_sel_hi:[1,0]
	v_cvt_pk_fp8_f32 v108, v104, v105 op_sel:[0,0,1]
	v_pk_mul_f32 v[104:105], v[106:107], s[8:9] op_sel_hi:[1,0]
	v_cvt_pk_fp8_f32 v111, v96, v97 op_sel:[0,0,1]
	v_lshl_add_u64 v[96:97], s[20:21], 0, v[130:131]
	v_cvt_pk_fp8_f32 v92, v88, v89 op_sel:[0,0,1]
	v_pk_mul_f32 v[88:89], v[90:91], s[8:9] op_sel_hi:[1,0]
	v_cvt_pk_fp8_f32 v60, v56, v57 op_sel:[0,0,1]
	v_pk_mul_f32 v[56:57], v[58:59], s[8:9] op_sel_hi:[1,0]
	v_cvt_pk_fp8_f32 v44, v40, v41 op_sel:[0,0,1]
	v_pk_mul_f32 v[40:41], v[42:43], s[8:9] op_sel_hi:[1,0]
	v_cvt_pk_fp8_f32 v46, v32, v33 op_sel:[0,0,1]
	v_pk_mul_f32 v[32:33], v[34:35], s[8:9] op_sel_hi:[1,0]
	s_add_u32 s16, s16, s35
	v_cvt_pk_fp8_f32 v28, v24, v25 op_sel:[0,0,1]
	v_pk_mul_f32 v[24:25], v[26:27], s[8:9] op_sel_hi:[1,0]
	v_pk_mul_f32 v[0:1], v[6:7], s[8:9] op_sel_hi:[1,0]
	v_cvt_pk_fp8_f32 v125, v120, v121 op_sel:[0,0,1]
	v_cvt_pk_fp8_f32 v109, v104, v105 op_sel:[0,0,1]
	v_lshl_add_u64 v[96:97], v[96:97], 0, v[128:129]
	v_cvt_pk_fp8_f32 v93, v88, v89 op_sel:[0,0,1]
	v_cvt_pk_fp8_f32 v76, v72, v73 op_sel:[0,0,1]
	v_pk_mul_f32 v[72:73], v[74:75], s[8:9] op_sel_hi:[1,0]
	v_cvt_pk_fp8_f32 v61, v56, v57 op_sel:[0,0,1]
	v_cvt_pk_fp8_f32 v45, v40, v41 op_sel:[0,0,1]
	v_cvt_pk_fp8_f32 v47, v32, v33 op_sel:[0,0,1]
	s_addc_u32 s17, s17, 0
	v_cvt_pk_fp8_f32 v29, v24, v25 op_sel:[0,0,1]
	v_cvt_pk_fp8_f32 v12, v8, v9 op_sel:[0,0,1]
	v_pk_mul_f32 v[8:9], v[10:11], s[8:9] op_sel_hi:[1,0]
	v_cvt_pk_fp8_f32 v14, v0, v1 op_sel:[0,0,1]
	v_pk_mul_f32 v[0:1], v[2:3], s[8:9] op_sel_hi:[1,0]
	v_add_co_u32_e32 v98, vcc, s30, v96
	v_cvt_pk_fp8_f32 v77, v72, v73 op_sel:[0,0,1]
	v_lshl_add_u64 v[32:33], s[16:17], 0, v[130:131]
	v_cvt_pk_fp8_f32 v13, v8, v9 op_sel:[0,0,1]
	v_cvt_pk_fp8_f32 v15, v0, v1 op_sel:[0,0,1]
	v_addc_co_u32_e32 v99, vcc, 0, v97, vcc
	v_lshl_add_u64 v[32:33], v[32:33], 0, v[128:129]
	v_add_co_u32_e32 v34, vcc, s30, v32
	v_permlane32_swap_b32_e32 v124, v126
	v_permlane32_swap_b32_e32 v125, v127
	v_permlane32_swap_b32_e32 v108, v110
	v_permlane32_swap_b32_e32 v109, v111
	v_permlane32_swap_b32_e32 v92, v94
	v_permlane32_swap_b32_e32 v93, v95
	v_permlane32_swap_b32_e32 v60, v62
	v_permlane32_swap_b32_e32 v61, v63
	v_permlane32_swap_b32_e32 v44, v46
	v_permlane32_swap_b32_e32 v45, v47
	v_addc_co_u32_e32 v35, vcc, 0, v33, vcc
	v_permlane32_swap_b32_e32 v28, v30
	v_permlane32_swap_b32_e32 v29, v31
	v_permlane16_swap_b32_e32 v124, v125
	v_permlane16_swap_b32_e32 v126, v127
	v_permlane16_swap_b32_e32 v108, v109
	v_permlane16_swap_b32_e32 v110, v111
	v_permlane16_swap_b32_e32 v92, v93
	v_permlane16_swap_b32_e32 v94, v95
	v_permlane32_swap_b32_e32 v76, v78
	v_permlane32_swap_b32_e32 v77, v79
	v_permlane16_swap_b32_e32 v60, v61
	v_permlane16_swap_b32_e32 v62, v63
	v_permlane16_swap_b32_e32 v44, v45
	v_permlane16_swap_b32_e32 v46, v47
	v_permlane16_swap_b32_e32 v28, v29
	v_permlane16_swap_b32_e32 v30, v31
	v_permlane32_swap_b32_e32 v12, v14
	v_permlane32_swap_b32_e32 v13, v15
	s_and_b64 vcc, exec, s[10:11]
	s_mov_b32 s51, s49
	s_mov_b32 s50, s48
	s_mov_b64 s[18:19], s[12:13]
	s_mov_b64 s[16:17], s[14:15]
	global_store_dwordx4 v[96:97], v[124:127], off
	global_store_dwordx4 v[98:99], v[108:111], off
	v_permlane16_swap_b32_e32 v76, v77
	v_permlane16_swap_b32_e32 v78, v79
	global_store_dwordx4 v[96:97], v[92:95], off offset:128
	global_store_dwordx4 v[98:99], v[76:79], off offset:128
	global_store_dwordx4 v[32:33], v[60:63], off
	global_store_dwordx4 v[34:35], v[44:47], off
	v_permlane16_swap_b32_e32 v12, v13
	v_permlane16_swap_b32_e32 v14, v15
	global_store_dwordx4 v[32:33], v[28:31], off offset:128
	global_store_dwordx4 v[34:35], v[12:15], off offset:128
	s_cbranch_vccz .LBB0_2377
	s_waitcnt vmcnt(0)
	v_readlane_b32 s0, v252, 2
	s_cmpk_gt_u32 s0, 0xff
	s_cbranch_scc1 .LBB0_2386
	s_barrier

.LBB0_4221:
	s_waitcnt vmcnt(31)
	v_mov_b32_e32 v128, v0
	s_waitcnt vmcnt(30)
	v_mov_b32_e32 v129, v4
	v_pk_mul_f32 v[128:129], v[128:129], s[68:69] op_sel_hi:[1,0]
	s_nop 0
	v_cvt_pk_fp8_f32 v130, v128, v129
	s_waitcnt vmcnt(29)
	v_mov_b32_e32 v128, v8
	s_waitcnt vmcnt(28)
	v_mov_b32_e32 v129, v12
	v_pk_mul_f32 v[128:129], v[128:129], s[68:69] op_sel_hi:[1,0]
	s_nop 0
	v_cvt_pk_fp8_f32 v130, v128, v129 op_sel:[0,0,1]
	v_mov_b32_e32 v128, v1
	v_mov_b32_e32 v129, v5
	v_pk_mul_f32 v[128:129], v[128:129], s[68:69] op_sel_hi:[1,0]
	s_nop 0
	v_cvt_pk_fp8_f32 v131, v128, v129
	v_mov_b32_e32 v128, v9
	v_mov_b32_e32 v129, v13
	v_pk_mul_f32 v[128:129], v[128:129], s[68:69] op_sel_hi:[1,0]
	s_nop 0
	v_cvt_pk_fp8_f32 v131, v128, v129 op_sel:[0,0,1]
	v_mov_b32_e32 v128, v2
	v_mov_b32_e32 v129, v6
	v_pk_mul_f32 v[128:129], v[128:129], s[68:69] op_sel_hi:[1,0]
	s_nop 0
	v_cvt_pk_fp8_f32 v136, v128, v129
	v_mov_b32_e32 v128, v10
	v_mov_b32_e32 v129, v14
	v_pk_mul_f32 v[128:129], v[128:129], s[68:69] op_sel_hi:[1,0]
	s_nop 0
	v_cvt_pk_fp8_f32 v136, v128, v129 op_sel:[0,0,1]
	v_mov_b32_e32 v128, v3
	v_mov_b32_e32 v129, v7
	v_pk_mul_f32 v[128:129], v[128:129], s[68:69] op_sel_hi:[1,0]
	v_add_u32_e32 v143, 0x4000, v141
	v_cvt_pk_fp8_f32 v137, v128, v129
	v_mov_b32_e32 v128, v11
	v_mov_b32_e32 v129, v15
	v_pk_mul_f32 v[128:129], v[128:129], s[68:69] op_sel_hi:[1,0]
	v_add_u32_e32 v142, 0x8400, v141
	v_cvt_pk_fp8_f32 v137, v128, v129 op_sel:[0,0,1]
	s_waitcnt vmcnt(27)
	v_mov_b32_e32 v128, v16
	s_waitcnt vmcnt(26)
	v_mov_b32_e32 v129, v20
	ds_write2_b32 v141, v130, v131 offset1:33
	ds_write2_b32 v141, v136, v137 offset0:66 offset1:99
	v_pk_mul_f32 v[128:129], v[128:129], s[68:69] op_sel_hi:[1,0]
	s_nop 0
	v_cvt_pk_fp8_f32 v130, v128, v129
	s_waitcnt vmcnt(25)
	v_mov_b32_e32 v128, v24
	s_waitcnt vmcnt(24)
	v_mov_b32_e32 v129, v28
	v_pk_mul_f32 v[128:129], v[128:129], s[68:69] op_sel_hi:[1,0]
	s_nop 0
	v_cvt_pk_fp8_f32 v130, v128, v129 op_sel:[0,0,1]
	v_mov_b32_e32 v128, v17
	v_mov_b32_e32 v129, v21
	v_pk_mul_f32 v[128:129], v[128:129], s[68:69] op_sel_hi:[1,0]
	s_nop 0
	v_cvt_pk_fp8_f32 v131, v128, v129
	v_mov_b32_e32 v128, v25
	v_mov_b32_e32 v129, v29
	v_pk_mul_f32 v[128:129], v[128:129], s[68:69] op_sel_hi:[1,0]
	s_nop 0
	v_cvt_pk_fp8_f32 v131, v128, v129 op_sel:[0,0,1]
	v_mov_b32_e32 v128, v18
	v_mov_b32_e32 v129, v22
	v_pk_mul_f32 v[128:129], v[128:129], s[68:69] op_sel_hi:[1,0]
	s_nop 0
	v_cvt_pk_fp8_f32 v136, v128, v129
	v_mov_b32_e32 v128, v26
	v_mov_b32_e32 v129, v30
	v_pk_mul_f32 v[128:129], v[128:129], s[68:69] op_sel_hi:[1,0]
	s_cmp_lt_i32 s66, 2
	v_cvt_pk_fp8_f32 v136, v128, v129 op_sel:[0,0,1]
	v_mov_b32_e32 v128, v19
	v_mov_b32_e32 v129, v23
	v_pk_mul_f32 v[128:129], v[128:129], s[68:69] op_sel_hi:[1,0]
	s_nop 0
	v_cvt_pk_fp8_f32 v137, v128, v129
	v_mov_b32_e32 v128, v27
	v_mov_b32_e32 v129, v31
	v_pk_mul_f32 v[128:129], v[128:129], s[68:69] op_sel_hi:[1,0]
	s_nop 0
	v_cvt_pk_fp8_f32 v137, v128, v129 op_sel:[0,0,1]
	s_waitcnt vmcnt(23)
	v_mov_b32_e32 v128, v48
	s_waitcnt vmcnt(22)
	v_mov_b32_e32 v129, v52
	v_pk_mul_f32 v[128:129], v[128:129], s[68:69] op_sel_hi:[1,0]
	ds_write2_b32 v143, v130, v131 offset0:128 offset1:161
	ds_write2_b32 v143, v136, v137 offset0:194 offset1:227
	v_cvt_pk_fp8_f32 v144, v128, v129
	s_waitcnt vmcnt(21)
	v_mov_b32_e32 v128, v56
	s_waitcnt vmcnt(20)
	v_mov_b32_e32 v129, v60
	v_pk_mul_f32 v[128:129], v[128:129], s[68:69] op_sel_hi:[1,0]
	s_nop 0
	v_cvt_pk_fp8_f32 v144, v128, v129 op_sel:[0,0,1]
	v_mov_b32_e32 v128, v49
	v_mov_b32_e32 v129, v53
	v_pk_mul_f32 v[128:129], v[128:129], s[68:69] op_sel_hi:[1,0]
	s_nop 0
	v_cvt_pk_fp8_f32 v145, v128, v129
	v_mov_b32_e32 v128, v57
	v_mov_b32_e32 v129, v61
	v_pk_mul_f32 v[128:129], v[128:129], s[68:69] op_sel_hi:[1,0]
	s_nop 0
	v_cvt_pk_fp8_f32 v145, v128, v129 op_sel:[0,0,1]
	v_mov_b32_e32 v128, v50
	v_mov_b32_e32 v129, v54
	v_pk_mul_f32 v[128:129], v[128:129], s[68:69] op_sel_hi:[1,0]
	s_nop 0
	v_cvt_pk_fp8_f32 v130, v128, v129
	v_mov_b32_e32 v128, v58
	v_mov_b32_e32 v129, v62
	v_pk_mul_f32 v[128:129], v[128:129], s[68:69] op_sel_hi:[1,0]
	ds_write2_b32 v142, v144, v145 offset1:33
	v_cvt_pk_fp8_f32 v130, v128, v129 op_sel:[0,0,1]
	v_mov_b32_e32 v128, v51
	v_mov_b32_e32 v129, v55
	v_pk_mul_f32 v[128:129], v[128:129], s[68:69] op_sel_hi:[1,0]
	s_nop 0
	v_cvt_pk_fp8_f32 v131, v128, v129
	v_mov_b32_e32 v128, v59
	v_mov_b32_e32 v129, v63
	v_pk_mul_f32 v[128:129], v[128:129], s[68:69] op_sel_hi:[1,0]
	v_add_u32_e32 v144, 0xc400, v141
	v_cvt_pk_fp8_f32 v131, v128, v129 op_sel:[0,0,1]
	s_waitcnt vmcnt(19)
	v_mov_b32_e32 v128, v96
	s_waitcnt vmcnt(18)
	v_mov_b32_e32 v129, v100
	v_pk_mul_f32 v[128:129], v[128:129], s[68:69] op_sel_hi:[1,0]
	ds_write2_b32 v142, v130, v131 offset0:66 offset1:99
	v_cvt_pk_fp8_f32 v136, v128, v129
	s_waitcnt vmcnt(17)
	v_mov_b32_e32 v128, v104
	s_waitcnt vmcnt(16)
	v_mov_b32_e32 v129, v108
	v_pk_mul_f32 v[128:129], v[128:129], s[68:69] op_sel_hi:[1,0]
	s_nop 0
	v_cvt_pk_fp8_f32 v136, v128, v129 op_sel:[0,0,1]
	v_mov_b32_e32 v128, v97
	v_mov_b32_e32 v129, v101
	v_pk_mul_f32 v[128:129], v[128:129], s[68:69] op_sel_hi:[1,0]
	s_nop 0
	v_cvt_pk_fp8_f32 v137, v128, v129
	v_mov_b32_e32 v128, v105
	v_mov_b32_e32 v129, v109
	v_pk_mul_f32 v[128:129], v[128:129], s[68:69] op_sel_hi:[1,0]
	s_nop 0
	v_cvt_pk_fp8_f32 v137, v128, v129 op_sel:[0,0,1]
	v_mov_b32_e32 v128, v98
	v_mov_b32_e32 v129, v102
	v_pk_mul_f32 v[128:129], v[128:129], s[68:69] op_sel_hi:[1,0]
	s_nop 0
	v_cvt_pk_fp8_f32 v145, v128, v129
	v_mov_b32_e32 v128, v106
	v_mov_b32_e32 v129, v110
	v_pk_mul_f32 v[128:129], v[128:129], s[68:69] op_sel_hi:[1,0]
	s_nop 0
	v_cvt_pk_fp8_f32 v145, v128, v129 op_sel:[0,0,1]
	v_mov_b32_e32 v128, v99
	v_mov_b32_e32 v129, v103
	v_pk_mul_f32 v[128:129], v[128:129], s[68:69] op_sel_hi:[1,0]
	s_nop 0
	v_cvt_pk_fp8_f32 v146, v128, v129
	v_mov_b32_e32 v128, v107
	v_mov_b32_e32 v129, v111
	v_pk_mul_f32 v[128:129], v[128:129], s[68:69] op_sel_hi:[1,0]
	s_nop 0
	v_cvt_pk_fp8_f32 v146, v128, v129 op_sel:[0,0,1]
	ds_write2_b32 v144, v136, v137 offset0:128 offset1:161
	ds_write2_b32 v144, v145, v146 offset0:194 offset1:227
	s_waitcnt lgkmcnt(0)
	s_barrier
	ds_read2_b32 v[128:129], v140 offset1:1
	ds_read2_b32 v[130:131], v140 offset0:2 offset1:3
	v_lshl_add_u32 v136, s65, 6, v138
	s_cbranch_scc1 .LBB0_4227
	s_cmp_gt_i32 s66, 2
	s_cbranch_scc0 .LBB0_4228
	s_cmp_eq_u32 s66, 3
	s_mov_b64 s[34:35], -1
	s_cbranch_scc0 .LBB0_4225
	v_lshlrev_b32_e32 v137, 1, v136
	v_and_b32_e32 v145, 0x7f, v136
	s_movk_i32 s11, 0xff00
	v_and_or_b32 v137, v137, s11, v145
	s_mov_b64 s[34:35], 0

.LBB0_4635:
	s_waitcnt vmcnt(31)
	v_mov_b32_e32 v130, v2
	s_waitcnt vmcnt(30)
	v_mov_b32_e32 v131, v6
	v_pk_mul_f32 v[130:131], v[130:131], s[64:65] op_sel_hi:[1,0]
	s_nop 0
	v_cvt_pk_fp8_f32 v132, v130, v131
	s_waitcnt vmcnt(29)
	v_mov_b32_e32 v130, v10
	s_waitcnt vmcnt(28)
	v_mov_b32_e32 v131, v14
	v_pk_mul_f32 v[130:131], v[130:131], s[64:65] op_sel_hi:[1,0]
	s_nop 0
	v_cvt_pk_fp8_f32 v132, v130, v131 op_sel:[0,0,1]
	v_mov_b32_e32 v130, v3
	v_mov_b32_e32 v131, v7
	v_pk_mul_f32 v[130:131], v[130:131], s[64:65] op_sel_hi:[1,0]
	s_nop 0
	v_cvt_pk_fp8_f32 v133, v130, v131
	v_mov_b32_e32 v130, v11
	v_mov_b32_e32 v131, v15
	v_pk_mul_f32 v[130:131], v[130:131], s[64:65] op_sel_hi:[1,0]
	s_nop 0
	v_cvt_pk_fp8_f32 v133, v130, v131 op_sel:[0,0,1]
	v_mov_b32_e32 v130, v4
	v_mov_b32_e32 v131, v8
	v_pk_mul_f32 v[130:131], v[130:131], s[64:65] op_sel_hi:[1,0]
	s_nop 0
	v_cvt_pk_fp8_f32 v136, v130, v131
	v_mov_b32_e32 v130, v12
	v_mov_b32_e32 v131, v16
	v_pk_mul_f32 v[130:131], v[130:131], s[64:65] op_sel_hi:[1,0]
	s_nop 0
	v_cvt_pk_fp8_f32 v136, v130, v131 op_sel:[0,0,1]
	v_mov_b32_e32 v130, v5
	v_mov_b32_e32 v131, v9
	v_pk_mul_f32 v[130:131], v[130:131], s[64:65] op_sel_hi:[1,0]
	v_add_u32_e32 v144, 0x4000, v142
	v_cvt_pk_fp8_f32 v137, v130, v131
	v_mov_b32_e32 v130, v13
	v_mov_b32_e32 v131, v17
	v_pk_mul_f32 v[130:131], v[130:131], s[64:65] op_sel_hi:[1,0]
	v_add_u32_e32 v143, 0x8400, v142
	v_cvt_pk_fp8_f32 v137, v130, v131 op_sel:[0,0,1]
	s_waitcnt vmcnt(27)
	v_mov_b32_e32 v130, v18
	s_waitcnt vmcnt(26)
	v_mov_b32_e32 v131, v22
	ds_write2_b32 v142, v132, v133 offset1:33
	ds_write2_b32 v142, v136, v137 offset0:66 offset1:99
	v_pk_mul_f32 v[130:131], v[130:131], s[64:65] op_sel_hi:[1,0]
	s_nop 0
	v_cvt_pk_fp8_f32 v132, v130, v131
	s_waitcnt vmcnt(25)
	v_mov_b32_e32 v130, v26
	s_waitcnt vmcnt(24)
	v_mov_b32_e32 v131, v30
	v_pk_mul_f32 v[130:131], v[130:131], s[64:65] op_sel_hi:[1,0]
	s_nop 0
	v_cvt_pk_fp8_f32 v132, v130, v131 op_sel:[0,0,1]
	v_mov_b32_e32 v130, v19
	v_mov_b32_e32 v131, v23
	v_pk_mul_f32 v[130:131], v[130:131], s[64:65] op_sel_hi:[1,0]
	s_nop 0
	v_cvt_pk_fp8_f32 v133, v130, v131
	v_mov_b32_e32 v130, v27
	v_mov_b32_e32 v131, v31
	v_pk_mul_f32 v[130:131], v[130:131], s[64:65] op_sel_hi:[1,0]
	s_nop 0
	v_cvt_pk_fp8_f32 v133, v130, v131 op_sel:[0,0,1]
	v_mov_b32_e32 v130, v20
	v_mov_b32_e32 v131, v24
	v_pk_mul_f32 v[130:131], v[130:131], s[64:65] op_sel_hi:[1,0]
	s_nop 0
	v_cvt_pk_fp8_f32 v136, v130, v131
	v_mov_b32_e32 v130, v28
	v_mov_b32_e32 v131, v32
	v_pk_mul_f32 v[130:131], v[130:131], s[64:65] op_sel_hi:[1,0]
	s_cmp_lt_i32 s66, 2
	v_cvt_pk_fp8_f32 v136, v130, v131 op_sel:[0,0,1]
	v_mov_b32_e32 v130, v21
	v_mov_b32_e32 v131, v25
	v_pk_mul_f32 v[130:131], v[130:131], s[64:65] op_sel_hi:[1,0]
	s_nop 0
	v_cvt_pk_fp8_f32 v137, v130, v131
	v_mov_b32_e32 v130, v29
	v_mov_b32_e32 v131, v33
	v_pk_mul_f32 v[130:131], v[130:131], s[64:65] op_sel_hi:[1,0]
	s_nop 0
	v_cvt_pk_fp8_f32 v137, v130, v131 op_sel:[0,0,1]
	s_waitcnt vmcnt(23)
	v_mov_b32_e32 v130, v50
	s_waitcnt vmcnt(22)
	v_mov_b32_e32 v131, v54
	v_pk_mul_f32 v[130:131], v[130:131], s[64:65] op_sel_hi:[1,0]
	ds_write2_b32 v144, v132, v133 offset0:128 offset1:161
	ds_write2_b32 v144, v136, v137 offset0:194 offset1:227
	v_cvt_pk_fp8_f32 v145, v130, v131
	s_waitcnt vmcnt(21)
	v_mov_b32_e32 v130, v74
	s_waitcnt vmcnt(20)
	v_mov_b32_e32 v131, v78
	v_pk_mul_f32 v[130:131], v[130:131], s[64:65] op_sel_hi:[1,0]
	s_nop 0
	v_cvt_pk_fp8_f32 v145, v130, v131 op_sel:[0,0,1]
	v_mov_b32_e32 v130, v51
	v_mov_b32_e32 v131, v55
	v_pk_mul_f32 v[130:131], v[130:131], s[64:65] op_sel_hi:[1,0]
	s_nop 0
	v_cvt_pk_fp8_f32 v146, v130, v131
	v_mov_b32_e32 v130, v75
	v_mov_b32_e32 v131, v79
	v_pk_mul_f32 v[130:131], v[130:131], s[64:65] op_sel_hi:[1,0]
	s_nop 0
	v_cvt_pk_fp8_f32 v146, v130, v131 op_sel:[0,0,1]
	v_mov_b32_e32 v130, v52
	v_mov_b32_e32 v131, v56
	v_pk_mul_f32 v[130:131], v[130:131], s[64:65] op_sel_hi:[1,0]
	s_nop 0
	v_cvt_pk_fp8_f32 v132, v130, v131
	v_mov_b32_e32 v130, v76
	v_mov_b32_e32 v131, v80
	v_pk_mul_f32 v[130:131], v[130:131], s[64:65] op_sel_hi:[1,0]
	ds_write2_b32 v143, v145, v146 offset1:33
	v_cvt_pk_fp8_f32 v132, v130, v131 op_sel:[0,0,1]
	v_mov_b32_e32 v130, v53
	v_mov_b32_e32 v131, v57
	v_pk_mul_f32 v[130:131], v[130:131], s[64:65] op_sel_hi:[1,0]
	s_nop 0
	v_cvt_pk_fp8_f32 v133, v130, v131
	v_mov_b32_e32 v130, v77
	v_mov_b32_e32 v131, v81
	v_pk_mul_f32 v[130:131], v[130:131], s[64:65] op_sel_hi:[1,0]
	v_add_u32_e32 v145, 0xc400, v142
	v_cvt_pk_fp8_f32 v133, v130, v131 op_sel:[0,0,1]
	s_waitcnt vmcnt(19)
	v_mov_b32_e32 v130, v98
	s_waitcnt vmcnt(18)
	v_mov_b32_e32 v131, v102
	v_pk_mul_f32 v[130:131], v[130:131], s[64:65] op_sel_hi:[1,0]
	ds_write2_b32 v143, v132, v133 offset0:66 offset1:99
	v_cvt_pk_fp8_f32 v136, v130, v131
	s_waitcnt vmcnt(17)
	v_mov_b32_e32 v130, v106
	s_waitcnt vmcnt(16)
	v_mov_b32_e32 v131, v110
	v_pk_mul_f32 v[130:131], v[130:131], s[64:65] op_sel_hi:[1,0]
	s_nop 0
	v_cvt_pk_fp8_f32 v136, v130, v131 op_sel:[0,0,1]
	v_mov_b32_e32 v130, v99
	v_mov_b32_e32 v131, v103
	v_pk_mul_f32 v[130:131], v[130:131], s[64:65] op_sel_hi:[1,0]
	s_nop 0
	v_cvt_pk_fp8_f32 v137, v130, v131
	v_mov_b32_e32 v130, v107
	v_mov_b32_e32 v131, v111
	v_pk_mul_f32 v[130:131], v[130:131], s[64:65] op_sel_hi:[1,0]
	s_nop 0
	v_cvt_pk_fp8_f32 v137, v130, v131 op_sel:[0,0,1]
	v_mov_b32_e32 v130, v100
	v_mov_b32_e32 v131, v104
	v_pk_mul_f32 v[130:131], v[130:131], s[64:65] op_sel_hi:[1,0]
	s_nop 0
	v_cvt_pk_fp8_f32 v146, v130, v131
	v_mov_b32_e32 v130, v108
	v_mov_b32_e32 v131, v112
	v_pk_mul_f32 v[130:131], v[130:131], s[64:65] op_sel_hi:[1,0]
	s_nop 0
	v_cvt_pk_fp8_f32 v146, v130, v131 op_sel:[0,0,1]
	v_mov_b32_e32 v130, v101
	v_mov_b32_e32 v131, v105
	v_pk_mul_f32 v[130:131], v[130:131], s[64:65] op_sel_hi:[1,0]
	s_nop 0
	v_cvt_pk_fp8_f32 v147, v130, v131
	v_mov_b32_e32 v130, v109
	v_mov_b32_e32 v131, v113
	v_pk_mul_f32 v[130:131], v[130:131], s[64:65] op_sel_hi:[1,0]
	s_nop 0
	v_cvt_pk_fp8_f32 v147, v130, v131 op_sel:[0,0,1]
	ds_write2_b32 v145, v136, v137 offset0:128 offset1:161
	ds_write2_b32 v145, v146, v147 offset0:194 offset1:227
	s_waitcnt lgkmcnt(0)
	s_barrier
	ds_read2_b32 v[130:131], v141 offset1:1
	ds_read2_b32 v[132:133], v141 offset0:2 offset1:3
	v_lshl_add_u32 v136, s67, 6, v139
	s_cbranch_scc1 .LBB0_4641
	s_cmp_gt_i32 s66, 2
	s_cbranch_scc0 .LBB0_4642
	s_cmp_eq_u32 s66, 3
	s_mov_b64 s[94:95], -1
	s_cbranch_scc0 .LBB0_4639
	v_lshlrev_b32_e32 v137, 1, v136
	v_and_b32_e32 v146, 0x7f, v136
	s_movk_i32 s19, 0xff00
	v_and_or_b32 v137, v137, s19, v146
	s_mov_b64 s[94:95], 0

.Lpf_skip_1:
	v_lshlrev_b32_e32 v90, 16, v88
	v_and_b32_e32 v91, 0xffff0000, v88
	v_sub_f32_e32 v90, v86, v90
	v_sub_f32_e32 v91, v87, v91
	v_cvt_pk_bf16_f32 v89, v84, v85
	v_cvt_pk_bf16_f32 v90, v90, v91
	v_lshlrev_b32_e32 v128, 4, v128
	v_lshlrev_b32_e32 v91, 16, v89
	v_sub_f32_e32 v91, v84, v91
	v_and_b32_e32 v129, 0xffff0000, v89
	v_add3_u32 v128, s46, v128, v228
	v_sub_f32_e32 v129, v85, v129
	v_cvt_pk_bf16_f32 v91, v91, v129
	ds_write_b64 v128, v[88:89]
	v_add_u32_e32 v88, 0x10000, v128
	ds_write_b64 v88, v[90:91]
	s_nop 0
	v_cvt_pk_fp8_f32 v90, v154, v155
	s_nop 0
	v_cvt_pk_fp8_f32 v91, v174, v175
	v_lshl_add_u64 v[88:89], s[6:7], 0, v[78:79]
	v_cvt_pk_fp8_f32 v90, v152, v153 op_sel:[0,0,1]
	s_nop 0
	v_cvt_pk_fp8_f32 v91, v170, v171 op_sel:[0,0,1]
	v_cvt_pk_fp8_f32 v128, v186, v187
	global_store_dword v[88:89], v90, off
	v_lshl_add_u64 v[88:89], s[6:7], 0, v[76:77]
	s_nop 0
	global_store_dword v[88:89], v91, off
	v_cvt_pk_fp8_f32 v90, v158, v159
	s_nop 0
	v_cvt_pk_fp8_f32 v91, v178, v179
	v_cvt_pk_fp8_f32 v128, v184, v185 op_sel:[0,0,1]
	v_cvt_pk_fp8_f32 v90, v156, v157 op_sel:[0,0,1]
	v_lshl_add_u64 v[88:89], s[6:7], 0, v[74:75]
	v_cvt_pk_fp8_f32 v91, v176, v177 op_sel:[0,0,1]
	global_store_dword v[88:89], v128, off
	v_lshl_add_u64 v[88:89], s[6:7], 0, v[72:73]
	s_nop 0
	global_store_dword v[88:89], v90, off
	v_lshl_add_u64 v[88:89], s[6:7], 0, v[70:71]
	v_cvt_pk_fp8_f32 v128, v134, v135
	global_store_dword v[88:89], v91, off
	s_nop 0
	v_cvt_pk_fp8_f32 v88, v144, v145
	s_nop 0
	v_cvt_pk_fp8_f32 v89, v80, v81
	v_cvt_pk_fp8_f32 v128, v130, v131 op_sel:[0,0,1]
	v_cvt_pk_fp8_f32 v88, v242, v243 op_sel:[0,0,1]
	v_lshl_add_u64 v[80:81], s[6:7], 0, v[68:69]
	v_cvt_pk_fp8_f32 v89, v82, v83 op_sel:[0,0,1]
	global_store_dword v[80:81], v128, off
	v_lshl_add_u64 v[80:81], s[6:7], 0, v[66:67]
	global_store_dword v[80:81], v88, off
	v_lshl_add_u64 v[80:81], s[6:7], 0, v[64:65]
	global_store_dword v[80:81], v89, off
	s_nop 0
	s_nop 0
	v_cvt_pk_fp8_f32 v80, v146, v147
	v_cvt_pk_fp8_f32 v81, v164, v165
	s_add_i32 s6, s1, s18
	s_ashr_i32 s7, s6, 31
	s_lshl_b64 s[6:7], s[6:7], 11
	v_cvt_pk_fp8_f32 v80, v142, v143 op_sel:[0,0,1]
	v_cvt_pk_fp8_f32 v81, v162, v163 op_sel:[0,0,1]
	s_add_u32 s6, s41, s6
	s_addc_u32 s7, s42, s7
	v_lshl_add_u64 v[78:79], s[6:7], 0, v[78:79]
	v_lshl_add_u64 v[76:77], s[6:7], 0, v[76:77]
	s_nop 0
	global_store_dword v[78:79], v80, off
	global_store_dword v[76:77], v81, off
	s_nop 0
	s_nop 0
	v_cvt_pk_fp8_f32 v82, v182, v183
	v_cvt_pk_fp8_f32 v76, v150, v151
	v_cvt_pk_fp8_f32 v77, v172, v173
	v_lshl_add_u64 v[74:75], s[6:7], 0, v[74:75]
	v_cvt_pk_fp8_f32 v82, v180, v181 op_sel:[0,0,1]
	v_cvt_pk_fp8_f32 v76, v148, v149 op_sel:[0,0,1]
	v_cvt_pk_fp8_f32 v77, v168, v169 op_sel:[0,0,1]
	v_lshl_add_u64 v[72:73], s[6:7], 0, v[72:73]
	v_lshl_add_u64 v[70:71], s[6:7], 0, v[70:71]
	global_store_dword v[74:75], v82, off
	s_nop 0
	global_store_dword v[72:73], v76, off
	global_store_dword v[70:71], v77, off
	s_nop 0
	s_nop 0
	v_cvt_pk_fp8_f32 v74, v94, v95
	v_cvt_pk_fp8_f32 v70, v138, v139
	v_cvt_pk_fp8_f32 v71, v86, v87
	v_lshl_add_u64 v[68:69], s[6:7], 0, v[68:69]
	v_cvt_pk_fp8_f32 v74, v92, v93 op_sel:[0,0,1]
	v_cvt_pk_fp8_f32 v70, v136, v137 op_sel:[0,0,1]
	v_cvt_pk_fp8_f32 v71, v84, v85 op_sel:[0,0,1]
	v_lshl_add_u64 v[66:67], s[6:7], 0, v[66:67]
	v_lshl_add_u64 v[64:65], s[6:7], 0, v[64:65]
	global_store_dword v[68:69], v74, off
	global_store_dword v[66:67], v70, off
	global_store_dword v[64:65], v71, off
	s_waitcnt lgkmcnt(0)
	s_barrier
	ds_read_b128 v[64:67], v190
	ds_read_b128 v[68:71], v191
	s_waitcnt lgkmcnt(1)
	v_mfma_f32_16x16x32_bf16 v[72:75], v[0:3], v[64:67], 0
	v_mov_b32_e32 v128, v167
	v_mfma_f32_16x16x32_bf16 v[64:67], v[4:7], v[64:67], v[72:75]
	s_waitcnt lgkmcnt(0)
	v_mfma_f32_16x16x32_bf16 v[64:67], v[0:3], v[68:71], v[64:67]
	ds_read_b128 v[68:71], v192
	s_nop 2
	ds_read_b128 v[72:75], v193
	s_waitcnt lgkmcnt(1)
	v_mfma_f32_16x16x32_bf16 v[64:67], v[8:11], v[68:71], v[64:67]
	v_mfma_f32_16x16x32_bf16 v[64:67], v[12:15], v[68:71], v[64:67]
	s_waitcnt lgkmcnt(0)
	v_mfma_f32_16x16x32_bf16 v[64:67], v[8:11], v[72:75], v[64:67]
	ds_read_b128 v[68:71], v194
	ds_read_b128 v[72:75], v195
	s_waitcnt lgkmcnt(1)
	v_mfma_f32_16x16x32_bf16 v[64:67], v[16:19], v[68:71], v[64:67]
	v_mfma_f32_16x16x32_bf16 v[64:67], v[20:23], v[68:71], v[64:67]
	s_waitcnt lgkmcnt(0)
	v_mfma_f32_16x16x32_bf16 v[64:67], v[16:19], v[72:75], v[64:67]
	ds_read_b128 v[68:71], v196
	ds_read_b128 v[72:75], v197
	s_waitcnt lgkmcnt(1)
	v_mfma_f32_16x16x32_bf16 v[64:67], v[24:27], v[68:71], v[64:67]
	v_mfma_f32_16x16x32_bf16 v[64:67], v[28:31], v[68:71], v[64:67]
	s_waitcnt lgkmcnt(0)
	v_mfma_f32_16x16x32_bf16 v[64:67], v[24:27], v[72:75], v[64:67]
	ds_read_b128 v[68:71], v198
	ds_read_b128 v[72:75], v199
	s_waitcnt lgkmcnt(1)
	v_mfma_f32_16x16x32_bf16 v[64:67], v[32:35], v[68:71], v[64:67]
	v_mfma_f32_16x16x32_bf16 v[64:67], v[36:39], v[68:71], v[64:67]
	s_waitcnt lgkmcnt(0)
	v_mfma_f32_16x16x32_bf16 v[64:67], v[32:35], v[72:75], v[64:67]
	ds_read_b128 v[68:71], v200
	ds_read_b128 v[72:75], v201
	s_waitcnt lgkmcnt(1)
	v_mfma_f32_16x16x32_bf16 v[64:67], v[40:43], v[68:71], v[64:67]
	v_mfma_f32_16x16x32_bf16 v[64:67], v[44:47], v[68:71], v[64:67]
	s_waitcnt lgkmcnt(0)
	v_mfma_f32_16x16x32_bf16 v[64:67], v[40:43], v[72:75], v[64:67]
	ds_read_b128 v[68:71], v202
	ds_read_b128 v[72:75], v203
	s_waitcnt lgkmcnt(1)
	v_mfma_f32_16x16x32_bf16 v[64:67], v[48:51], v[68:71], v[64:67]
	v_mfma_f32_16x16x32_bf16 v[64:67], v[52:55], v[68:71], v[64:67]
	s_waitcnt lgkmcnt(0)
	v_mfma_f32_16x16x32_bf16 v[64:67], v[48:51], v[72:75], v[64:67]
	ds_read_b128 v[68:71], v204
	ds_read_b128 v[72:75], v205
	s_waitcnt lgkmcnt(1)
	v_mfma_f32_16x16x32_bf16 v[64:67], v[56:59], v[68:71], v[64:67]
	v_mfma_f32_16x16x32_bf16 v[64:67], v[60:63], v[68:71], v[64:67]
	s_waitcnt lgkmcnt(0)
	v_mfma_f32_16x16x32_bf16 v[64:67], v[56:59], v[72:75], v[64:67]
	s_nop 7
	ds_write_b128 v208, v[64:67]
	s_waitcnt lgkmcnt(0)
	s_barrier
	s_nop 0
	v_cmp_gt_i32_e32 vcc, s48, v128
	s_and_saveexec_b64 s[6:7], vcc
	s_cbranch_execz .LBB0_5172
	v_lshl_add_u32 v72, v128, 2, 0
	v_add_u32_e32 v70, 0x22000, v72
	ds_read2st64_b32 v[64:65], v70 offset1:4
	ds_read2st64_b32 v[66:67], v70 offset0:8 offset1:12
	ds_read2st64_b32 v[68:69], v70 offset0:16 offset1:20
	ds_read2st64_b32 v[70:71], v70 offset0:24 offset1:28
	s_waitcnt lgkmcnt(3)
	v_add_f32_e32 v64, 0, v64
	v_add_f32_e32 v64, v64, v65
	s_waitcnt lgkmcnt(2)
	v_add_f32_e32 v64, v64, v66
	v_add_f32_e32 v64, v64, v67
	s_waitcnt lgkmcnt(1)
	v_add_f32_e32 v64, v64, v68
	v_add_f32_e32 v64, v64, v69
	s_waitcnt lgkmcnt(0)
	v_add_f32_e32 v64, v64, v70
	v_add_f32_e32 v64, v64, v71
	v_add_u32_e32 v65, 0x21000, v72
	ds_write_b32 v65, v64
	v_mul_f32_e32 v142, 0xbfb8aa3b, v64
	v_fma_f32 v143, v64, s50, -v142
	v_rndne_f32_e32 v144, v142
	v_fmac_f32_e32 v143, 0xb2a5705f, v64
	v_sub_f32_e32 v142, v142, v144
	v_add_f32_e32 v142, v142, v143
	v_cvt_i32_f32_e32 v145, v144
	v_exp_f32_e32 v146, v142
	v_cmp_nlt_f32_e32 vcc, s51, v64
	v_ldexp_f32 v145, v146, v145
	s_nop 0
	v_cndmask_b32_e32 v145, 0, v145, vcc
	v_cmp_ngt_f32_e32 vcc, s52, v64
	s_nop 1
	v_cndmask_b32_e32 v145, v211, v145, vcc
	v_add_f32_e32 v145, 1.0, v145
	v_div_scale_f32 v146, s[98:99], v145, v145, 1.0
	v_rcp_f32_e32 v147, v146
	v_div_scale_f32 v148, vcc, 1.0, v145, 1.0
	v_fma_f32 v149, -v146, v147, 1.0
	v_fmac_f32_e32 v147, v149, v147
	v_mul_f32_e32 v149, v148, v147
	v_fma_f32 v150, -v146, v149, v148
	v_fmac_f32_e32 v149, v150, v147
	v_fma_f32 v146, -v146, v149, v148
	v_div_fmas_f32 v146, v146, v147, v149
	v_div_fixup_f32 v146, v146, v145, 1.0
	ds_write_b32 v65, v146 offset:1024
	v_add_f32_e32 v147, v249, v146
	ds_write_b32 v65, v147 offset:2048

.LBB0_5513:
	s_waitcnt vmcnt(31)
	v_mov_b32_e32 v128, v0
	s_waitcnt vmcnt(30)
	v_mov_b32_e32 v129, v4
	v_pk_mul_f32 v[128:129], v[128:129], s[40:41] op_sel_hi:[1,0]
	s_nop 0
	v_cvt_pk_fp8_f32 v130, v128, v129
	s_waitcnt vmcnt(29)
	v_mov_b32_e32 v128, v8
	s_waitcnt vmcnt(28)
	v_mov_b32_e32 v129, v12
	v_pk_mul_f32 v[128:129], v[128:129], s[40:41] op_sel_hi:[1,0]
	s_nop 0
	v_cvt_pk_fp8_f32 v130, v128, v129 op_sel:[0,0,1]
	v_mov_b32_e32 v128, v1
	v_mov_b32_e32 v129, v5
	v_pk_mul_f32 v[128:129], v[128:129], s[40:41] op_sel_hi:[1,0]
	s_nop 0
	v_cvt_pk_fp8_f32 v131, v128, v129
	v_mov_b32_e32 v128, v9
	v_mov_b32_e32 v129, v13
	v_pk_mul_f32 v[128:129], v[128:129], s[40:41] op_sel_hi:[1,0]
	s_nop 0
	v_cvt_pk_fp8_f32 v131, v128, v129 op_sel:[0,0,1]
	v_mov_b32_e32 v128, v2
	v_mov_b32_e32 v129, v6
	v_pk_mul_f32 v[128:129], v[128:129], s[40:41] op_sel_hi:[1,0]
	s_nop 0
	v_cvt_pk_fp8_f32 v134, v128, v129
	v_mov_b32_e32 v128, v10
	v_mov_b32_e32 v129, v14
	v_pk_mul_f32 v[128:129], v[128:129], s[40:41] op_sel_hi:[1,0]
	s_nop 0
	v_cvt_pk_fp8_f32 v134, v128, v129 op_sel:[0,0,1]
	v_mov_b32_e32 v128, v3
	v_mov_b32_e32 v129, v7
	v_pk_mul_f32 v[128:129], v[128:129], s[40:41] op_sel_hi:[1,0]
	v_add_u32_e32 v145, 0x4000, v143
	v_cvt_pk_fp8_f32 v138, v128, v129
	v_mov_b32_e32 v128, v11
	v_mov_b32_e32 v129, v15
	v_pk_mul_f32 v[128:129], v[128:129], s[40:41] op_sel_hi:[1,0]
	v_add_u32_e32 v144, 0x8400, v143
	v_cvt_pk_fp8_f32 v138, v128, v129 op_sel:[0,0,1]
	s_waitcnt vmcnt(27)
	v_mov_b32_e32 v128, v16
	s_waitcnt vmcnt(26)
	v_mov_b32_e32 v129, v20
	ds_write2_b32 v143, v130, v131 offset1:33
	ds_write2_b32 v143, v134, v138 offset0:66 offset1:99
	v_pk_mul_f32 v[128:129], v[128:129], s[40:41] op_sel_hi:[1,0]
	s_nop 0
	v_cvt_pk_fp8_f32 v130, v128, v129
	s_waitcnt vmcnt(25)
	v_mov_b32_e32 v128, v24
	s_waitcnt vmcnt(24)
	v_mov_b32_e32 v129, v28
	v_pk_mul_f32 v[128:129], v[128:129], s[40:41] op_sel_hi:[1,0]
	s_nop 0
	v_cvt_pk_fp8_f32 v130, v128, v129 op_sel:[0,0,1]
	v_mov_b32_e32 v128, v17
	v_mov_b32_e32 v129, v21
	v_pk_mul_f32 v[128:129], v[128:129], s[40:41] op_sel_hi:[1,0]
	s_nop 0
	v_cvt_pk_fp8_f32 v131, v128, v129
	v_mov_b32_e32 v128, v25
	v_mov_b32_e32 v129, v29
	v_pk_mul_f32 v[128:129], v[128:129], s[40:41] op_sel_hi:[1,0]
	s_nop 0
	v_cvt_pk_fp8_f32 v131, v128, v129 op_sel:[0,0,1]
	v_mov_b32_e32 v128, v18
	v_mov_b32_e32 v129, v22
	v_pk_mul_f32 v[128:129], v[128:129], s[40:41] op_sel_hi:[1,0]
	s_nop 0
	v_cvt_pk_fp8_f32 v134, v128, v129
	v_mov_b32_e32 v128, v26
	v_mov_b32_e32 v129, v30
	v_pk_mul_f32 v[128:129], v[128:129], s[40:41] op_sel_hi:[1,0]
	s_cmp_lt_i32 s73, 2
	v_cvt_pk_fp8_f32 v134, v128, v129 op_sel:[0,0,1]
	v_mov_b32_e32 v128, v19
	v_mov_b32_e32 v129, v23
	v_pk_mul_f32 v[128:129], v[128:129], s[40:41] op_sel_hi:[1,0]
	s_nop 0
	v_cvt_pk_fp8_f32 v138, v128, v129
	v_mov_b32_e32 v128, v27
	v_mov_b32_e32 v129, v31
	v_pk_mul_f32 v[128:129], v[128:129], s[40:41] op_sel_hi:[1,0]
	s_nop 0
	v_cvt_pk_fp8_f32 v138, v128, v129 op_sel:[0,0,1]
	s_waitcnt vmcnt(23)
	v_mov_b32_e32 v128, v48
	s_waitcnt vmcnt(22)
	v_mov_b32_e32 v129, v52
	v_pk_mul_f32 v[128:129], v[128:129], s[40:41] op_sel_hi:[1,0]
	ds_write2_b32 v145, v130, v131 offset0:128 offset1:161
	ds_write2_b32 v145, v134, v138 offset0:194 offset1:227
	v_cvt_pk_fp8_f32 v139, v128, v129
	s_waitcnt vmcnt(21)
	v_mov_b32_e32 v128, v56
	s_waitcnt vmcnt(20)
	v_mov_b32_e32 v129, v60
	v_pk_mul_f32 v[128:129], v[128:129], s[40:41] op_sel_hi:[1,0]
	s_nop 0
	v_cvt_pk_fp8_f32 v139, v128, v129 op_sel:[0,0,1]
	v_mov_b32_e32 v128, v49
	v_mov_b32_e32 v129, v53
	v_pk_mul_f32 v[128:129], v[128:129], s[40:41] op_sel_hi:[1,0]
	s_nop 0
	v_cvt_pk_fp8_f32 v146, v128, v129
	v_mov_b32_e32 v128, v57
	v_mov_b32_e32 v129, v61
	v_pk_mul_f32 v[128:129], v[128:129], s[40:41] op_sel_hi:[1,0]
	s_nop 0
	v_cvt_pk_fp8_f32 v146, v128, v129 op_sel:[0,0,1]
	v_mov_b32_e32 v128, v50
	v_mov_b32_e32 v129, v54
	v_pk_mul_f32 v[128:129], v[128:129], s[40:41] op_sel_hi:[1,0]
	s_nop 0
	v_cvt_pk_fp8_f32 v130, v128, v129
	v_mov_b32_e32 v128, v58
	v_mov_b32_e32 v129, v62
	v_pk_mul_f32 v[128:129], v[128:129], s[40:41] op_sel_hi:[1,0]
	ds_write2_b32 v144, v139, v146 offset1:33
	v_cvt_pk_fp8_f32 v130, v128, v129 op_sel:[0,0,1]
	v_mov_b32_e32 v128, v51
	v_mov_b32_e32 v129, v55
	v_pk_mul_f32 v[128:129], v[128:129], s[40:41] op_sel_hi:[1,0]
	s_nop 0
	v_cvt_pk_fp8_f32 v131, v128, v129
	v_mov_b32_e32 v128, v59
	v_mov_b32_e32 v129, v63
	v_pk_mul_f32 v[128:129], v[128:129], s[40:41] op_sel_hi:[1,0]
	v_add_u32_e32 v146, 0xc400, v143
	v_cvt_pk_fp8_f32 v131, v128, v129 op_sel:[0,0,1]
	s_waitcnt vmcnt(19)
	v_mov_b32_e32 v128, v96
	s_waitcnt vmcnt(18)
	v_mov_b32_e32 v129, v100
	v_pk_mul_f32 v[128:129], v[128:129], s[40:41] op_sel_hi:[1,0]
	ds_write2_b32 v144, v130, v131 offset0:66 offset1:99
	v_cvt_pk_fp8_f32 v134, v128, v129
	s_waitcnt vmcnt(17)
	v_mov_b32_e32 v128, v104
	s_waitcnt vmcnt(16)
	v_mov_b32_e32 v129, v108
	v_pk_mul_f32 v[128:129], v[128:129], s[40:41] op_sel_hi:[1,0]
	s_nop 0
	v_cvt_pk_fp8_f32 v134, v128, v129 op_sel:[0,0,1]
	v_mov_b32_e32 v128, v97
	v_mov_b32_e32 v129, v101
	v_pk_mul_f32 v[128:129], v[128:129], s[40:41] op_sel_hi:[1,0]
	s_nop 0
	v_cvt_pk_fp8_f32 v138, v128, v129
	v_mov_b32_e32 v128, v105
	v_mov_b32_e32 v129, v109
	v_pk_mul_f32 v[128:129], v[128:129], s[40:41] op_sel_hi:[1,0]
	s_nop 0
	v_cvt_pk_fp8_f32 v138, v128, v129 op_sel:[0,0,1]
	v_mov_b32_e32 v128, v98
	v_mov_b32_e32 v129, v102
	v_pk_mul_f32 v[128:129], v[128:129], s[40:41] op_sel_hi:[1,0]
	s_nop 0
	v_cvt_pk_fp8_f32 v139, v128, v129
	v_mov_b32_e32 v128, v106
	v_mov_b32_e32 v129, v110
	v_pk_mul_f32 v[128:129], v[128:129], s[40:41] op_sel_hi:[1,0]
	s_nop 0
	v_cvt_pk_fp8_f32 v139, v128, v129 op_sel:[0,0,1]
	v_mov_b32_e32 v128, v99
	v_mov_b32_e32 v129, v103
	v_pk_mul_f32 v[128:129], v[128:129], s[40:41] op_sel_hi:[1,0]
	s_nop 0
	v_cvt_pk_fp8_f32 v147, v128, v129
	v_mov_b32_e32 v128, v107
	v_mov_b32_e32 v129, v111
	v_pk_mul_f32 v[128:129], v[128:129], s[40:41] op_sel_hi:[1,0]
	s_nop 0
	v_cvt_pk_fp8_f32 v147, v128, v129 op_sel:[0,0,1]
	ds_write2_b32 v146, v134, v138 offset0:128 offset1:161
	ds_write2_b32 v146, v139, v147 offset0:194 offset1:227
	s_waitcnt lgkmcnt(0)
	s_barrier
	ds_read2_b32 v[128:129], v142 offset1:1
	ds_read2_b32 v[130:131], v142 offset0:2 offset1:3
	v_lshl_add_u32 v134, s72, 6, v140
	s_cbranch_scc1 .LBB0_5519
	s_cmp_gt_i32 s73, 2
	s_cbranch_scc0 .LBB0_5520
	s_cmp_eq_u32 s73, 3
	s_mov_b64 s[68:69], -1
	s_cbranch_scc0 .LBB0_5517
	v_lshlrev_b32_e32 v138, 1, v134
	v_and_b32_e32 v139, 0x7f, v134
	s_movk_i32 s19, 0xff00
	v_and_or_b32 v138, v138, s19, v139
	s_mov_b64 s[68:69], 0

.Lpeel_exit_9:
	v_pk_mul_f32 v[140:141], v[124:125], s[6:7] op_sel_hi:[1,0]
	v_pk_mul_f32 v[120:121], v[120:121], s[6:7] op_sel_hi:[1,0]
	s_nop 0
	v_cvt_pk_fp8_f32 v125, v120, v121
	v_pk_mul_f32 v[120:121], v[126:127], s[6:7] op_sel_hi:[1,0]
	v_pk_mul_f32 v[116:117], v[116:117], s[6:7] op_sel_hi:[1,0]
	s_nop 0
	v_cvt_pk_fp8_f32 v126, v116, v117
	v_pk_mul_f32 v[112:113], v[112:113], s[6:7] op_sel_hi:[1,0]
	s_nop 0
	v_cvt_pk_fp8_f32 v127, v112, v113
	v_pk_mul_f32 v[112:113], v[118:119], s[6:7] op_sel_hi:[1,0]
	v_pk_mul_f32 v[104:105], v[104:105], s[6:7] op_sel_hi:[1,0]
	v_cvt_pk_fp8_f32 v126, v112, v113 op_sel:[0,0,1]
	v_pk_mul_f32 v[112:113], v[114:115], s[6:7] op_sel_hi:[1,0]
	v_pk_mul_f32 v[100:101], v[100:101], s[6:7] op_sel_hi:[1,0]
	v_cvt_pk_fp8_f32 v127, v112, v113 op_sel:[0,0,1]
	v_pk_mul_f32 v[112:113], v[108:109], s[6:7] op_sel_hi:[1,0]
	s_nop 0
	v_cvt_pk_fp8_f32 v109, v104, v105
	v_pk_mul_f32 v[104:105], v[110:111], s[6:7] op_sel_hi:[1,0]
	s_nop 0
	v_cvt_pk_fp8_f32 v110, v100, v101
	v_pk_mul_f32 v[100:101], v[92:93], s[6:7] op_sel_hi:[1,0]
	v_pk_mul_f32 v[88:89], v[88:89], s[6:7] op_sel_hi:[1,0]
	s_nop 0
	v_cvt_pk_fp8_f32 v93, v88, v89
	v_pk_mul_f32 v[88:89], v[94:95], s[6:7] op_sel_hi:[1,0]
	v_pk_mul_f32 v[84:85], v[84:85], s[6:7] op_sel_hi:[1,0]
	s_nop 0
	v_cvt_pk_fp8_f32 v94, v84, v85
	v_pk_mul_f32 v[80:81], v[80:81], s[6:7] op_sel_hi:[1,0]
	s_nop 0
	v_cvt_pk_fp8_f32 v95, v80, v81
	v_pk_mul_f32 v[80:81], v[86:87], s[6:7] op_sel_hi:[1,0]
	v_pk_mul_f32 v[72:73], v[72:73], s[6:7] op_sel_hi:[1,0]
	v_cvt_pk_fp8_f32 v94, v80, v81 op_sel:[0,0,1]
	v_pk_mul_f32 v[80:81], v[82:83], s[6:7] op_sel_hi:[1,0]
	v_pk_mul_f32 v[68:69], v[68:69], s[6:7] op_sel_hi:[1,0]
	v_cvt_pk_fp8_f32 v95, v80, v81 op_sel:[0,0,1]
	v_pk_mul_f32 v[80:81], v[76:77], s[6:7] op_sel_hi:[1,0]
	s_nop 0
	v_cvt_pk_fp8_f32 v77, v72, v73
	v_pk_mul_f32 v[72:73], v[78:79], s[6:7] op_sel_hi:[1,0]
	s_nop 0
	v_cvt_pk_fp8_f32 v78, v68, v69
	v_pk_mul_f32 v[64:65], v[64:65], s[6:7] op_sel_hi:[1,0]
	s_nop 0
	v_cvt_pk_fp8_f32 v79, v64, v65
	v_pk_mul_f32 v[64:65], v[70:71], s[6:7] op_sel_hi:[1,0]
	v_pk_mul_f32 v[56:57], v[56:57], s[6:7] op_sel_hi:[1,0]
	v_cvt_pk_fp8_f32 v78, v64, v65 op_sel:[0,0,1]
	v_pk_mul_f32 v[64:65], v[66:67], s[6:7] op_sel_hi:[1,0]
	v_pk_mul_f32 v[52:53], v[52:53], s[6:7] op_sel_hi:[1,0]
	v_cvt_pk_fp8_f32 v79, v64, v65 op_sel:[0,0,1]
	v_pk_mul_f32 v[64:65], v[60:61], s[6:7] op_sel_hi:[1,0]
	s_nop 0
	v_cvt_pk_fp8_f32 v61, v56, v57
	v_pk_mul_f32 v[56:57], v[62:63], s[6:7] op_sel_hi:[1,0]
	s_nop 0
	v_cvt_pk_fp8_f32 v62, v52, v53
	v_pk_mul_f32 v[48:49], v[48:49], s[6:7] op_sel_hi:[1,0]
	s_nop 0
	v_cvt_pk_fp8_f32 v63, v48, v49
	s_lshl_b32 s14, s49, 8
	v_pk_mul_f32 v[48:49], v[54:55], s[6:7] op_sel_hi:[1,0]
	s_add_i32 s14, s14, s33
	v_cvt_pk_fp8_f32 v62, v48, v49 op_sel:[0,0,1]
	v_pk_mul_f32 v[48:49], v[50:51], s[6:7] op_sel_hi:[1,0]
	s_lshl_b32 s16, s50, 8
	s_ashr_i32 s15, s14, 31
	v_cvt_pk_fp8_f32 v63, v48, v49 op_sel:[0,0,1]
	v_pk_mul_f32 v[48:49], v[44:45], s[6:7] op_sel_hi:[1,0]
	v_pk_mul_f32 v[40:41], v[40:41], s[6:7] op_sel_hi:[1,0]
	s_nop 0
	s_ashr_i32 s17, s16, 31
	s_lshl_b64 s[18:19], s[14:15], 11
	v_cvt_pk_fp8_f32 v45, v40, v41
	v_pk_mul_f32 v[40:41], v[46:47], s[6:7] op_sel_hi:[1,0]
	v_pk_mul_f32 v[36:37], v[36:37], s[6:7] op_sel_hi:[1,0]
	s_nop 0
	s_add_u32 s15, s30, s18
	v_cvt_pk_fp8_f32 v46, v36, v37
	v_pk_mul_f32 v[36:37], v[28:29], s[6:7] op_sel_hi:[1,0]
	v_pk_mul_f32 v[24:25], v[24:25], s[6:7] op_sel_hi:[1,0]
	s_nop 0
	s_addc_u32 s18, s31, s19
	v_cvt_pk_fp8_f32 v29, v24, v25
	v_pk_mul_f32 v[24:25], v[30:31], s[6:7] op_sel_hi:[1,0]
	v_pk_mul_f32 v[20:21], v[20:21], s[6:7] op_sel_hi:[1,0]
	s_nop 0
	s_add_u32 s15, s15, s16
	v_cvt_pk_fp8_f32 v30, v20, v21
	v_pk_mul_f32 v[16:17], v[16:17], s[6:7] op_sel_hi:[1,0]
	s_nop 0
	s_addc_u32 s19, s18, s17
	v_cvt_pk_fp8_f32 v31, v16, v17
	s_add_u32 s18, s15, s34
	s_addc_u32 s19, s19, 0
	s_addk_i32 s14, 0x80
	v_pk_mul_f32 v[16:17], v[22:23], s[6:7] op_sel_hi:[1,0]
	s_ashr_i32 s15, s14, 31
	v_cvt_pk_fp8_f32 v30, v16, v17 op_sel:[0,0,1]
	v_pk_mul_f32 v[16:17], v[18:19], s[6:7] op_sel_hi:[1,0]
	s_nop 0
	s_nop 0
	v_pk_mul_f32 v[96:97], v[96:97], s[6:7] op_sel_hi:[1,0]
	s_nop 0
	s_nop 0
	s_lshl_b64 s[14:15], s[14:15], 11
	s_nop 0
	s_nop 0
	s_nop 0
	v_cvt_pk_fp8_f32 v31, v16, v17 op_sel:[0,0,1]
	v_pk_mul_f32 v[16:17], v[12:13], s[6:7] op_sel_hi:[1,0]
	v_pk_mul_f32 v[8:9], v[8:9], s[6:7] op_sel_hi:[1,0]
	s_nop 0
	v_mbcnt_lo_u32_b32 v128, -1, 0
	v_mbcnt_hi_u32_b32 v128, -1, v128
	v_cvt_pk_fp8_f32 v124, v140, v141
	v_ashrrev_i32_e32 v130, 1, v128
	v_cvt_pk_fp8_f32 v108, v112, v113
	v_cvt_pk_fp8_f32 v111, v96, v97
	v_cvt_pk_fp8_f32 v92, v100, v101
	s_nop 0
	v_cvt_pk_fp8_f32 v60, v64, v65
	v_cvt_pk_fp8_f32 v44, v48, v49
	v_pk_mul_f32 v[32:33], v[32:33], s[6:7] op_sel_hi:[1,0]
	s_nop 0
	s_add_u32 s14, s30, s14
	v_cvt_pk_fp8_f32 v28, v36, v37
	s_nop 0
	v_cvt_pk_fp8_f32 v13, v8, v9
	v_pk_mul_f32 v[8:9], v[14:15], s[6:7] op_sel_hi:[1,0]
	v_pk_mul_f32 v[4:5], v[4:5], s[6:7] op_sel_hi:[1,0]
	s_nop 0
	v_bfi_b32 v130, -16, v130, v128
	v_cvt_pk_fp8_f32 v76, v80, v81
	v_cvt_pk_fp8_f32 v47, v32, v33
	s_addc_u32 s15, s31, s15
	v_cvt_pk_fp8_f32 v12, v16, v17
	v_cvt_pk_fp8_f32 v14, v4, v5
	v_pk_mul_f32 v[0:1], v[0:1], s[6:7] op_sel_hi:[1,0]
	s_nop 0
	v_ashrrev_i32_e32 v131, 31, v130
	v_pk_mul_f32 v[96:97], v[102:103], s[6:7] op_sel_hi:[1,0]
	s_add_u32 s14, s14, s16
	v_cvt_pk_fp8_f32 v15, v0, v1
	v_lshlrev_b64 v[130:131], 11, v[130:131]
	v_cvt_pk_fp8_f32 v110, v96, v97 op_sel:[0,0,1]
	v_pk_mul_f32 v[96:97], v[98:99], s[6:7] op_sel_hi:[1,0]
	v_pk_mul_f32 v[32:33], v[38:39], s[6:7] op_sel_hi:[1,0]
	s_addc_u32 s15, s15, s17
	v_and_b32_e32 v128, 16, v128
	v_cvt_pk_fp8_f32 v124, v120, v121 op_sel:[0,0,1]
	v_pk_mul_f32 v[120:121], v[122:123], s[6:7] op_sel_hi:[1,0]
	v_cvt_pk_fp8_f32 v108, v104, v105 op_sel:[0,0,1]
	v_pk_mul_f32 v[104:105], v[106:107], s[6:7] op_sel_hi:[1,0]
	v_cvt_pk_fp8_f32 v111, v96, v97 op_sel:[0,0,1]
	v_lshl_add_u64 v[96:97], s[18:19], 0, v[130:131]
	v_cvt_pk_fp8_f32 v92, v88, v89 op_sel:[0,0,1]
	v_pk_mul_f32 v[88:89], v[90:91], s[6:7] op_sel_hi:[1,0]
	v_cvt_pk_fp8_f32 v60, v56, v57 op_sel:[0,0,1]
	v_pk_mul_f32 v[56:57], v[58:59], s[6:7] op_sel_hi:[1,0]
	v_cvt_pk_fp8_f32 v44, v40, v41 op_sel:[0,0,1]
	v_pk_mul_f32 v[40:41], v[42:43], s[6:7] op_sel_hi:[1,0]
	v_cvt_pk_fp8_f32 v46, v32, v33 op_sel:[0,0,1]
	v_pk_mul_f32 v[32:33], v[34:35], s[6:7] op_sel_hi:[1,0]
	s_add_u32 s14, s14, s34
	v_cvt_pk_fp8_f32 v28, v24, v25 op_sel:[0,0,1]
	v_pk_mul_f32 v[24:25], v[26:27], s[6:7] op_sel_hi:[1,0]
	v_pk_mul_f32 v[0:1], v[6:7], s[6:7] op_sel_hi:[1,0]
	v_cvt_pk_fp8_f32 v125, v120, v121 op_sel:[0,0,1]
	v_cvt_pk_fp8_f32 v109, v104, v105 op_sel:[0,0,1]
	v_lshl_add_u64 v[96:97], v[96:97], 0, v[128:129]
	v_cvt_pk_fp8_f32 v93, v88, v89 op_sel:[0,0,1]
	v_cvt_pk_fp8_f32 v76, v72, v73 op_sel:[0,0,1]
	v_pk_mul_f32 v[72:73], v[74:75], s[6:7] op_sel_hi:[1,0]
	v_cvt_pk_fp8_f32 v61, v56, v57 op_sel:[0,0,1]
	v_cvt_pk_fp8_f32 v45, v40, v41 op_sel:[0,0,1]
	v_cvt_pk_fp8_f32 v47, v32, v33 op_sel:[0,0,1]
	s_addc_u32 s15, s15, 0
	v_cvt_pk_fp8_f32 v29, v24, v25 op_sel:[0,0,1]
	v_cvt_pk_fp8_f32 v12, v8, v9 op_sel:[0,0,1]
	v_pk_mul_f32 v[8:9], v[10:11], s[6:7] op_sel_hi:[1,0]
	v_cvt_pk_fp8_f32 v14, v0, v1 op_sel:[0,0,1]
	v_pk_mul_f32 v[0:1], v[2:3], s[6:7] op_sel_hi:[1,0]
	v_add_co_u32_e32 v98, vcc, s29, v96
	v_cvt_pk_fp8_f32 v77, v72, v73 op_sel:[0,0,1]
	v_lshl_add_u64 v[32:33], s[14:15], 0, v[130:131]
	v_cvt_pk_fp8_f32 v13, v8, v9 op_sel:[0,0,1]
	v_cvt_pk_fp8_f32 v15, v0, v1 op_sel:[0,0,1]
	v_addc_co_u32_e32 v99, vcc, 0, v97, vcc
	v_lshl_add_u64 v[32:33], v[32:33], 0, v[128:129]
	v_add_co_u32_e32 v34, vcc, s29, v32
	v_permlane32_swap_b32_e32 v124, v126
	v_permlane32_swap_b32_e32 v125, v127
	v_permlane32_swap_b32_e32 v108, v110
	v_permlane32_swap_b32_e32 v109, v111
	v_permlane32_swap_b32_e32 v92, v94
	v_permlane32_swap_b32_e32 v93, v95
	v_permlane32_swap_b32_e32 v60, v62
	v_permlane32_swap_b32_e32 v61, v63
	v_permlane32_swap_b32_e32 v44, v46
	v_permlane32_swap_b32_e32 v45, v47
	v_addc_co_u32_e32 v35, vcc, 0, v33, vcc
	v_permlane32_swap_b32_e32 v28, v30
	v_permlane32_swap_b32_e32 v29, v31
	v_permlane16_swap_b32_e32 v124, v125
	v_permlane16_swap_b32_e32 v126, v127
	v_permlane16_swap_b32_e32 v108, v109
	v_permlane16_swap_b32_e32 v110, v111
	v_permlane16_swap_b32_e32 v92, v93
	v_permlane16_swap_b32_e32 v94, v95
	v_permlane32_swap_b32_e32 v76, v78
	v_permlane32_swap_b32_e32 v77, v79
	v_permlane16_swap_b32_e32 v60, v61
	v_permlane16_swap_b32_e32 v62, v63
	v_permlane16_swap_b32_e32 v44, v45
	v_permlane16_swap_b32_e32 v46, v47
	v_permlane16_swap_b32_e32 v28, v29
	v_permlane16_swap_b32_e32 v30, v31
	v_permlane32_swap_b32_e32 v12, v14
	v_permlane32_swap_b32_e32 v13, v15
	s_and_b64 vcc, exec, s[8:9]
	s_mov_b32 s50, s48
	s_mov_b32 s49, s47
	s_mov_b64 s[16:17], s[10:11]
	s_mov_b64 s[14:15], s[12:13]
	global_store_dwordx4 v[96:97], v[124:127], off
	global_store_dwordx4 v[98:99], v[108:111], off
	v_permlane16_swap_b32_e32 v76, v77
	v_permlane16_swap_b32_e32 v78, v79
	global_store_dwordx4 v[96:97], v[92:95], off offset:128
	global_store_dwordx4 v[98:99], v[76:79], off offset:128
	global_store_dwordx4 v[32:33], v[60:63], off
	global_store_dwordx4 v[34:35], v[44:47], off
	v_permlane16_swap_b32_e32 v12, v13
	v_permlane16_swap_b32_e32 v14, v15
	global_store_dwordx4 v[32:33], v[28:31], off offset:128
	global_store_dwordx4 v[34:35], v[12:15], off offset:128
	s_cbranch_vccz .LBB0_5808
	s_waitcnt vmcnt(0)
	v_readlane_b32 s0, v252, 2
	s_cmpk_gt_u32 s0, 0xff
	s_cbranch_scc1 .LBB0_5817
	s_barrier
